# P10: per-step row offsets fetched with one s_load_dwordx16 from a per-wave list in d_ws (sorted, pre-shifted; 2 stores per token) instead of 32 v_readlane + lane-index s_adds + per-step vector select/
# speedup vs baseline: 1.0183x; 1.0142x over previous
; #define EXP_ROW(src, l) (*(const u32x4*)(UV + ((unsigned)__builtin_amdgcn_readlane((src), (l)) * 1024u + lo16)))
; #define EXP_XROW(tt) do { const char* g_ = (const char*)(xin + (size_t)(tt) * 1024) + lane * 16; LAS unsigned char* l_ = xslot + ((tt) & 1) * 2048; \
;         __builtin_amdgcn_global_load_lds((const unsigned*)g_, (LAS unsigned*)l_, 16, 0, 2); __builtin_amdgcn_global_load_lds((const unsigned*)(g_ + 1024), (LAS unsigned*)(l_ + 1024), 16, 0, 2); } while (0)
; __device__ __forceinline__ void expert_tokens(const unsigned char* __restrict__ UV, const float* __restrict__ US, const float* __restrict__ VS, ...
;     if (t0 >= t1) return;
;     const unsigned lo16 = (unsigned)lane * 16u;
;     const int el = ((lane >> 5) & 1) * 8 + ((lane >> 4) & 1) * 4 + ((lane >> 1) & 1) * 2 + (lane & 1);
;     const unsigned cw0 = (unsigned)IDX[(size_t)t0 * 128 + lane], cw1 = (unsigned)IDX[(size_t)t0 * 128 + 64 + lane];
;     int ci0 = (int)cw0 & rmask, ci1 = (int)cw1 & rmask;
;     float cg0 = __uint_as_float(cw0 & 0xFFFF0000u), cg1 = __uint_as_float(cw1 & 0xFFFF0000u);
;     float csu0 = US[ci0], csu1 = US[ci1], csv0 = VS[ci0], csv1 = VS[ci1];
;     ...
;     EXP_XROW(t0);
;     u32x4 A[EB], B[EB];
; #pragma unroll
;     for (int e = 0; e < EB; ++e) A[e] = EXP_ROW(ci0, e);
; #pragma unroll
;     for (int e = 0; e < EB; ++e) B[e] = EXP_ROW(ci0, EB + e);
.LBB0_1011:
	s_or_b64 exec, exec, s[12:13]
	s_waitcnt lgkmcnt(0)
	s_mul_i32 s8, s24, s96
	s_add_i32 s0, s8, s24
	s_min_i32 s17, s0, 0x8000
	s_sub_i32 s84, s96, s95
	s_add_i32 s84, s84, 8
	s_mul_i32 s84, s84, s24
	s_cmp_le_i32 s84, 0x8000
	s_cselect_b32 s84, 1, 0
	s_cmp_ge_i32 s8, s17
	s_waitcnt vmcnt(0)
	s_barrier
	s_cbranch_scc1 .LBB0_1025
	s_add_u32 s0, s6, 0xf800000
	s_addc_u32 s1, s7, 0
	s_add_u32 s10, s6, 0x1200000
	s_addc_u32 s11, s7, 0
	s_mov_b32 s80, s10
	s_and_b32 s81, s11, 0xffff
	s_mov_b32 s82, 0x1000000
	s_mov_b32 s83, 0x20000
	s_mov_b32 s32, 0xf000f0
	s_lshl_b32 s92, s96, 10
	s_add_u32 s86, s6, s92
	s_addc_u32 s87, s7, 0
	s_add_u32 s86, s86, 0x3500000
	s_addc_u32 s87, s87, 0
	s_add_u32 s88, s86, 0x200
	s_addc_u32 s89, s87, 0
	s_add_u32 s12, s6, 0x1100000
	s_addc_u32 s13, s7, 0
	s_add_u32 s14, s6, 0x1140000
	s_addc_u32 s15, s7, 0
	s_lshl_b32 s2, s95, 12
	s_add_i32 s26, s2, 0
	s_add_u32 s2, s6, 0x1b800000
	s_addc_u32 s3, s7, 0
	s_ashr_i32 s9, s8, 31
	s_lshl_b64 s[6:7], s[8:9], 9
	v_and_b32_e32 v74, 63, v0
	s_add_u32 s6, s0, s6
	s_addc_u32 s7, s1, s7
	v_lshlrev_b32_e32 v192, 2, v74
	global_load_dword v229, v192, s[6:7]
	global_load_dword v230, v192, s[6:7] offset:256
	s_lshl_b64 s[18:19], s[8:9], 11
	s_add_u32 s18, s2, s18
	s_addc_u32 s19, s3, s19
	s_lshl_b32 s9, s8, 11
	v_mov_b32_e32 v1, 0
	s_and_b32 s9, s9, 0x800
	v_lshlrev_b32_e32 v194, 4, v74
	v_mov_b32_e32 v195, v1
	s_add_i32 s9, s26, s9
	s_mov_b64 s[6:7], 0x400
	v_lshl_add_u64 v[2:3], s[18:19], 0, v[194:195]
	s_add_i32 m0, s9, 0x4000
	v_lshl_add_u64 v[2:3], v[2:3], 0, s[6:7]
	global_load_lds_dwordx4 v194, s[18:19] nt
	s_add_i32 m0, s9, 0x4400
	v_mov_b32_e32 v193, v1
	global_load_lds_dwordx4 v[2:3], off nt
	v_and_b32_e32 v77, 2, v0
	v_lshl_add_u64 v[196:197], s[0:1], 0, v[192:193]
	v_lshl_add_u64 v[198:199], s[2:3], 0, v[194:195]
	v_cmp_eq_u32_e64 s[0:1], 0, v77
	v_lshl_add_u64 v[200:201], s[4:5], 0, v[194:195]
	v_lshl_add_u32 v195, v74, 3, s26
	v_mov_b32_e32 v226, 0x358637bd
	v_mov_b32_e32 v227, 0xbf3a00e3
	s_waitcnt vmcnt(0)
	v_alignbit_b32 v229, v229, v229, 16
	v_alignbit_b32 v230, v230, v230, 16
	s_nop 1
	s_mov_b32 s58, 0x99999999
	s_mov_b32 s59, 0x99999999
	v_min_u32_dpp v202, v229, v229 quad_perm:[1,0,3,2] row_mask:0xf bank_mask:0xf
	v_max_u32_dpp v203, v229, v229 quad_perm:[1,0,3,2] row_mask:0xf bank_mask:0xf
	v_min_u32_dpp v204, v230, v230 quad_perm:[1,0,3,2] row_mask:0xf bank_mask:0xf
	v_max_u32_dpp v205, v230, v230 quad_perm:[1,0,3,2] row_mask:0xf bank_mask:0xf
	v_cndmask_b32_e64 v229, v203, v202, s[58:59]
	v_cndmask_b32_e64 v230, v205, v204, s[58:59]
	s_mov_b32 s58, 0xcc33cc33
	s_mov_b32 s59, 0xcc33cc33
	v_min_u32_dpp v202, v229, v229 quad_perm:[2,3,0,1] row_mask:0xf bank_mask:0xf
	v_max_u32_dpp v203, v229, v229 quad_perm:[2,3,0,1] row_mask:0xf bank_mask:0xf
	v_min_u32_dpp v204, v230, v230 quad_perm:[2,3,0,1] row_mask:0xf bank_mask:0xf
	v_max_u32_dpp v205, v230, v230 quad_perm:[2,3,0,1] row_mask:0xf bank_mask:0xf
	v_cndmask_b32_e64 v229, v203, v202, s[58:59]
	v_cndmask_b32_e64 v230, v205, v204, s[58:59]
	s_mov_b32 s58, 0xaa55aa55
	s_mov_b32 s59, 0xaa55aa55
	v_min_u32_dpp v202, v229, v229 quad_perm:[1,0,3,2] row_mask:0xf bank_mask:0xf
	v_max_u32_dpp v203, v229, v229 quad_perm:[1,0,3,2] row_mask:0xf bank_mask:0xf
	v_min_u32_dpp v204, v230, v230 quad_perm:[1,0,3,2] row_mask:0xf bank_mask:0xf
	v_max_u32_dpp v205, v230, v230 quad_perm:[1,0,3,2] row_mask:0xf bank_mask:0xf
	v_cndmask_b32_e64 v229, v203, v202, s[58:59]
	v_cndmask_b32_e64 v230, v205, v204, s[58:59]
	s_mov_b32 s58, 0xf00ff00f
	s_mov_b32 s59, 0xf00ff00f
	v_min_u32_dpp v202, v229, v229 row_ror:8 row_mask:0xf bank_mask:0xf
	v_max_u32_dpp v203, v229, v229 row_ror:8 row_mask:0xf bank_mask:0xf
	v_min_u32_dpp v204, v230, v230 row_ror:8 row_mask:0xf bank_mask:0xf
	v_max_u32_dpp v205, v230, v230 row_ror:8 row_mask:0xf bank_mask:0xf
	v_cndmask_b32_e64 v229, v203, v202, s[58:59]
	v_cndmask_b32_e64 v230, v205, v204, s[58:59]
	s_mov_b32 s58, 0xc3c3c3c3
	s_mov_b32 s59, 0xc3c3c3c3
	v_min_u32_dpp v202, v229, v229 quad_perm:[2,3,0,1] row_mask:0xf bank_mask:0xf
	v_max_u32_dpp v203, v229, v229 quad_perm:[2,3,0,1] row_mask:0xf bank_mask:0xf
	v_min_u32_dpp v204, v230, v230 quad_perm:[2,3,0,1] row_mask:0xf bank_mask:0xf
	v_max_u32_dpp v205, v230, v230 quad_perm:[2,3,0,1] row_mask:0xf bank_mask:0xf
	v_cndmask_b32_e64 v229, v203, v202, s[58:59]
	v_cndmask_b32_e64 v230, v205, v204, s[58:59]
	s_mov_b32 s58, 0xa5a5a5a5
	s_mov_b32 s59, 0xa5a5a5a5
	v_min_u32_dpp v202, v229, v229 quad_perm:[1,0,3,2] row_mask:0xf bank_mask:0xf
	v_max_u32_dpp v203, v229, v229 quad_perm:[1,0,3,2] row_mask:0xf bank_mask:0xf
	v_min_u32_dpp v204, v230, v230 quad_perm:[1,0,3,2] row_mask:0xf bank_mask:0xf
	v_max_u32_dpp v205, v230, v230 quad_perm:[1,0,3,2] row_mask:0xf bank_mask:0xf
	v_cndmask_b32_e64 v229, v203, v202, s[58:59]
	v_cndmask_b32_e64 v230, v205, v204, s[58:59]
	s_mov_b32 s58, 0xf0f00f0f
	s_mov_b32 s59, 0xf0f00f0f
	v_mov_b32_dpp v202, v229 row_half_mirror row_mask:0xf bank_mask:0xf
	v_mov_b32_dpp v204, v230 row_half_mirror row_mask:0xf bank_mask:0xf
	s_nop 0
	v_max_u32_dpp v203, v202, v229 quad_perm:[3,2,1,0] row_mask:0xf bank_mask:0xf
	v_max_u32_dpp v205, v204, v230 quad_perm:[3,2,1,0] row_mask:0xf bank_mask:0xf
	v_min_u32_dpp v202, v202, v229 quad_perm:[3,2,1,0] row_mask:0xf bank_mask:0xf
	v_min_u32_dpp v204, v204, v230 quad_perm:[3,2,1,0] row_mask:0xf bank_mask:0xf
	v_cndmask_b32_e64 v229, v203, v202, s[58:59]
	v_cndmask_b32_e64 v230, v205, v204, s[58:59]
	s_mov_b32 s58, 0xff0000ff
	s_mov_b32 s59, 0xff0000ff
	v_min_u32_dpp v202, v229, v229 row_ror:8 row_mask:0xf bank_mask:0xf
	v_max_u32_dpp v203, v229, v229 row_ror:8 row_mask:0xf bank_mask:0xf
; __device__ __forceinline__ void expert_tokens(const unsigned char* __restrict__ UV, const float* __restrict__ US, const float* __restrict__ VS, ...
;     ...
;     const unsigned cw0 = (unsigned)IDX[(size_t)t0 * 128 + lane], cw1 = (unsigned)IDX[(size_t)t0 * 128 + 64 + lane];
;     int ci0 = (int)cw0 & rmask, ci1 = (int)cw1 & rmask;
;     float cg0 = __uint_as_float(cw0 & 0xFFFF0000u), cg1 = __uint_as_float(cw1 & 0xFFFF0000u);
	v_min_u32_dpp v204, v230, v230 row_ror:8 row_mask:0xf bank_mask:0xf
	v_max_u32_dpp v205, v230, v230 row_ror:8 row_mask:0xf bank_mask:0xf
	v_cndmask_b32_e64 v229, v203, v202, s[58:59]
	v_cndmask_b32_e64 v230, v205, v204, s[58:59]
	s_mov_b32 s58, 0xcccc3333
	s_mov_b32 s59, 0xcccc3333
	v_min_u32_dpp v202, v229, v229 quad_perm:[2,3,0,1] row_mask:0xf bank_mask:0xf
	v_max_u32_dpp v203, v229, v229 quad_perm:[2,3,0,1] row_mask:0xf bank_mask:0xf
	v_min_u32_dpp v204, v230, v230 quad_perm:[2,3,0,1] row_mask:0xf bank_mask:0xf
	v_max_u32_dpp v205, v230, v230 quad_perm:[2,3,0,1] row_mask:0xf bank_mask:0xf
	v_cndmask_b32_e64 v229, v203, v202, s[58:59]
	v_cndmask_b32_e64 v230, v205, v204, s[58:59]
	s_mov_b32 s58, 0xaaaa5555
	s_mov_b32 s59, 0xaaaa5555
	v_min_u32_dpp v202, v229, v229 quad_perm:[1,0,3,2] row_mask:0xf bank_mask:0xf
	v_max_u32_dpp v203, v229, v229 quad_perm:[1,0,3,2] row_mask:0xf bank_mask:0xf
	v_min_u32_dpp v204, v230, v230 quad_perm:[1,0,3,2] row_mask:0xf bank_mask:0xf
	v_max_u32_dpp v205, v230, v230 quad_perm:[1,0,3,2] row_mask:0xf bank_mask:0xf
	v_cndmask_b32_e64 v229, v203, v202, s[58:59]
	v_cndmask_b32_e64 v230, v205, v204, s[58:59]
	s_nop 1
	v_permlane16_swap_b32_e32 v229, v230
	s_mov_b32 s58, -1
	s_mov_b32 s59, 0
	v_min_u32_e32 v202, v229, v230
	v_max_u32_e32 v203, v229, v230
	v_cndmask_b32_e64 v229, v203, v202, s[58:59]
	v_cndmask_b32_e64 v230, v202, v203, s[58:59]
	s_mov_b32 s58, 0xf0f0f0f
	s_mov_b32 s59, 0xf0f0f0f0
	v_mov_b32_dpp v202, v229 row_half_mirror row_mask:0xf bank_mask:0xf
	v_mov_b32_dpp v204, v230 row_half_mirror row_mask:0xf bank_mask:0xf
	s_nop 0
	v_max_u32_dpp v203, v202, v229 quad_perm:[3,2,1,0] row_mask:0xf bank_mask:0xf
	v_max_u32_dpp v205, v204, v230 quad_perm:[3,2,1,0] row_mask:0xf bank_mask:0xf
	v_min_u32_dpp v202, v202, v229 quad_perm:[3,2,1,0] row_mask:0xf bank_mask:0xf
	v_min_u32_dpp v204, v204, v230 quad_perm:[3,2,1,0] row_mask:0xf bank_mask:0xf
	v_cndmask_b32_e64 v229, v203, v202, s[58:59]
	v_cndmask_b32_e64 v230, v205, v204, s[58:59]
	s_mov_b32 s58, 0xff00ff
	s_mov_b32 s59, 0xff00ff00
	v_min_u32_dpp v202, v229, v229 row_ror:8 row_mask:0xf bank_mask:0xf
	v_max_u32_dpp v203, v229, v229 row_ror:8 row_mask:0xf bank_mask:0xf
	v_min_u32_dpp v204, v230, v230 row_ror:8 row_mask:0xf bank_mask:0xf
	v_max_u32_dpp v205, v230, v230 row_ror:8 row_mask:0xf bank_mask:0xf
	v_cndmask_b32_e64 v229, v203, v202, s[58:59]
	v_cndmask_b32_e64 v230, v205, v204, s[58:59]
	s_mov_b32 s58, 0x33333333
	s_mov_b32 s59, 0xcccccccc
	v_min_u32_dpp v202, v229, v229 quad_perm:[2,3,0,1] row_mask:0xf bank_mask:0xf
	v_max_u32_dpp v203, v229, v229 quad_perm:[2,3,0,1] row_mask:0xf bank_mask:0xf
	v_min_u32_dpp v204, v230, v230 quad_perm:[2,3,0,1] row_mask:0xf bank_mask:0xf
	v_max_u32_dpp v205, v230, v230 quad_perm:[2,3,0,1] row_mask:0xf bank_mask:0xf
	v_cndmask_b32_e64 v229, v203, v202, s[58:59]
	v_cndmask_b32_e64 v230, v205, v204, s[58:59]
	s_mov_b32 s58, 0x55555555
	s_mov_b32 s59, 0xaaaaaaaa
	v_min_u32_dpp v202, v229, v229 quad_perm:[1,0,3,2] row_mask:0xf bank_mask:0xf
	v_max_u32_dpp v203, v229, v229 quad_perm:[1,0,3,2] row_mask:0xf bank_mask:0xf
	v_min_u32_dpp v204, v230, v230 quad_perm:[1,0,3,2] row_mask:0xf bank_mask:0xf
	v_max_u32_dpp v205, v230, v230 quad_perm:[1,0,3,2] row_mask:0xf bank_mask:0xf
	v_cndmask_b32_e64 v229, v203, v202, s[58:59]
	v_cndmask_b32_e64 v230, v205, v204, s[58:59]
	s_nop 1
	v_permlane32_swap_b32_e32 v229, v230
	s_mov_b32 s58, 0xffff
	s_mov_b32 s59, 0xffff
	v_min_u32_e32 v202, v229, v230
	v_max_u32_e32 v203, v229, v230
	v_cndmask_b32_e64 v229, v203, v202, s[58:59]
	v_cndmask_b32_e64 v230, v202, v203, s[58:59]
	s_nop 1
	v_permlane32_swap_b32_e32 v229, v230
	s_mov_b32 s58, 0xffff
	s_mov_b32 s59, 0xffff
	v_min_u32_e32 v202, v229, v230
	v_max_u32_e32 v203, v229, v230
	v_cndmask_b32_e64 v229, v203, v202, s[58:59]
	v_cndmask_b32_e64 v230, v202, v203, s[58:59]
	s_mov_b32 s58, 0xf0f00f0f
	s_mov_b32 s59, 0xf0f00f0f
	v_mov_b32_dpp v202, v229 row_half_mirror row_mask:0xf bank_mask:0xf
	v_mov_b32_dpp v204, v230 row_half_mirror row_mask:0xf bank_mask:0xf
	s_nop 0
	v_max_u32_dpp v203, v202, v229 quad_perm:[3,2,1,0] row_mask:0xf bank_mask:0xf
	v_max_u32_dpp v205, v204, v230 quad_perm:[3,2,1,0] row_mask:0xf bank_mask:0xf
	v_min_u32_dpp v202, v202, v229 quad_perm:[3,2,1,0] row_mask:0xf bank_mask:0xf
	v_min_u32_dpp v204, v204, v230 quad_perm:[3,2,1,0] row_mask:0xf bank_mask:0xf
	v_cndmask_b32_e64 v229, v203, v202, s[58:59]
	v_cndmask_b32_e64 v230, v205, v204, s[58:59]
	s_mov_b32 s58, 0xff0000ff
	s_mov_b32 s59, 0xff0000ff
	v_min_u32_dpp v202, v229, v229 row_ror:8 row_mask:0xf bank_mask:0xf
	v_max_u32_dpp v203, v229, v229 row_ror:8 row_mask:0xf bank_mask:0xf
	v_min_u32_dpp v204, v230, v230 row_ror:8 row_mask:0xf bank_mask:0xf
	v_max_u32_dpp v205, v230, v230 row_ror:8 row_mask:0xf bank_mask:0xf
	v_cndmask_b32_e64 v229, v203, v202, s[58:59]
	v_cndmask_b32_e64 v230, v205, v204, s[58:59]
	s_mov_b32 s58, 0xcccc3333
	s_mov_b32 s59, 0xcccc3333
	v_min_u32_dpp v202, v229, v229 quad_perm:[2,3,0,1] row_mask:0xf bank_mask:0xf
	v_max_u32_dpp v203, v229, v229 quad_perm:[2,3,0,1] row_mask:0xf bank_mask:0xf
	v_min_u32_dpp v204, v230, v230 quad_perm:[2,3,0,1] row_mask:0xf bank_mask:0xf
	v_max_u32_dpp v205, v230, v230 quad_perm:[2,3,0,1] row_mask:0xf bank_mask:0xf
	v_cndmask_b32_e64 v229, v203, v202, s[58:59]
	v_cndmask_b32_e64 v230, v205, v204, s[58:59]
	s_mov_b32 s58, 0xaaaa5555
	s_mov_b32 s59, 0xaaaa5555
	v_min_u32_dpp v202, v229, v229 quad_perm:[1,0,3,2] row_mask:0xf bank_mask:0xf
	v_max_u32_dpp v203, v229, v229 quad_perm:[1,0,3,2] row_mask:0xf bank_mask:0xf
	v_min_u32_dpp v204, v230, v230 quad_perm:[1,0,3,2] row_mask:0xf bank_mask:0xf
; #define EXP_ROW(src, l) (*(const u32x4*)(UV + ((unsigned)__builtin_amdgcn_readlane((src), (l)) * 1024u + lo16)))
; #define EXP_XROW(tt) do { const char* g_ = (const char*)(xin + (size_t)(tt) * 1024) + lane * 16; LAS unsigned char* l_ = xslot + ((tt) & 1) * 2048; \
;         __builtin_amdgcn_global_load_lds((const unsigned*)g_, (LAS unsigned*)l_, 16, 0, 2); __builtin_amdgcn_global_load_lds((const unsigned*)(g_ + 1024), (LAS unsigned*)(l_ + 1024), 16, 0, 2); } while (0)
; __device__ __forceinline__ void expert_tokens(const unsigned char* __restrict__ UV, const float* __restrict__ US, const float* __restrict__ VS, ...
;     ...
;     const unsigned cw0 = (unsigned)IDX[(size_t)t0 * 128 + lane], cw1 = (unsigned)IDX[(size_t)t0 * 128 + 64 + lane];
;     int ci0 = (int)cw0 & rmask, ci1 = (int)cw1 & rmask;
;     float cg0 = __uint_as_float(cw0 & 0xFFFF0000u), cg1 = __uint_as_float(cw1 & 0xFFFF0000u);
;     float csu0 = US[ci0], csu1 = US[ci1], csv0 = VS[ci0], csv1 = VS[ci1];
;     ...
;     EXP_XROW(t0);
;     u32x4 A[EB], B[EB];
; #pragma unroll
;     for (int e = 0; e < EB; ++e) A[e] = EXP_ROW(ci0, e);
; #pragma unroll
;     for (int e = 0; e < EB; ++e) B[e] = EXP_ROW(ci0, EB + e);
	v_max_u32_dpp v205, v230, v230 quad_perm:[1,0,3,2] row_mask:0xf bank_mask:0xf
	v_cndmask_b32_e64 v229, v203, v202, s[58:59]
	v_cndmask_b32_e64 v230, v205, v204, s[58:59]
	s_nop 1
	v_permlane16_swap_b32_e32 v229, v230
	v_min_u32_e32 v202, v229, v230
	v_max_u32_e32 v230, v229, v230
	v_mov_b32_e32 v229, v202
	s_nop 1
	v_permlane32_swap_b32_e32 v229, v230
	v_min_u32_e32 v202, v229, v230
	v_max_u32_e32 v230, v229, v230
	v_mov_b32_e32 v229, v202
	s_nop 1
	v_permlane16_swap_b32_e32 v229, v230
	v_min_u32_e32 v202, v229, v230
	v_max_u32_e32 v230, v229, v230
	v_mov_b32_e32 v229, v202
	s_nop 1
	v_permlane16_swap_b32_e32 v229, v230
	s_nop 1
	v_permlane32_swap_b32_e32 v229, v230
	v_alignbit_b32 v229, v229, v229, 16
	v_alignbit_b32 v230, v230, v230, 16
	v_and_b32_e32 v231, 0x3fff, v229
	v_and_b32_e32 v232, 0x3fff, v230
	v_lshlrev_b32_e32 v2, 10, v231
	v_lshlrev_b32_e32 v3, 10, v232
	global_store_dword v192, v2, s[86:87]
	global_store_dword v192, v3, s[86:87] offset:256
	v_readlane_b32 s40, v231, 22
	v_readlane_b32 s41, v231, 23
	v_readlane_b32 s49, v231, 31
	v_lshlrev_b32_e32 v2, 2, v231
	v_lshlrev_b32_e32 v3, 2, v232
	v_readlane_b32 s33, v231, 15
	v_readlane_b32 s34, v231, 16
	v_readlane_b32 s35, v231, 17
	v_readlane_b32 s36, v231, 18
	v_readlane_b32 s37, v231, 19
	v_readlane_b32 s38, v231, 20
	v_readlane_b32 s39, v231, 21
	v_readlane_b32 s42, v231, 24
	v_readlane_b32 s43, v231, 25
	v_readlane_b32 s44, v231, 26
	v_readlane_b32 s45, v231, 27
	v_readlane_b32 s46, v231, 28
	v_readlane_b32 s47, v231, 29
	v_readlane_b32 s48, v231, 30
	v_lshl_or_b32 v42, s49, 10, v194
	v_lshl_or_b32 v50, s41, 10, v194
	v_lshl_or_b32 v51, s40, 10, v194
	v_readlane_b32 s30, v231, 13
	v_readlane_b32 s31, v231, 14
	global_load_dword v233, v2, s[12:13]
	global_load_dword v234, v3, s[12:13]
	global_load_dword v236, v3, s[14:15]
	global_load_dword v235, v2, s[14:15]
	v_lshl_or_b32 v43, s48, 10, v194
	v_lshl_or_b32 v44, s47, 10, v194
	v_lshl_or_b32 v45, s46, 10, v194
	v_lshl_or_b32 v46, s45, 10, v194
	v_lshl_or_b32 v47, s44, 10, v194
	v_lshl_or_b32 v48, s43, 10, v194
	v_lshl_or_b32 v49, s42, 10, v194
	global_load_dwordx4 v[2:5], v42, s[10:11]
	global_load_dwordx4 v[10:13], v43, s[10:11]
	global_load_dwordx4 v[6:9], v44, s[10:11]
	global_load_dwordx4 v[18:21], v45, s[10:11]
	global_load_dwordx4 v[14:17], v46, s[10:11]
	global_load_dwordx4 v[26:29], v47, s[10:11]
	global_load_dwordx4 v[22:25], v48, s[10:11]
	global_load_dwordx4 v[34:37], v49, s[10:11]
	global_load_dwordx4 v[30:33], v50, s[10:11]
	global_load_dwordx4 v[38:41], v51, s[10:11]
	v_lshl_or_b32 v50, s39, 10, v194
	v_lshl_or_b32 v51, s38, 10, v194
	v_lshl_or_b32 v58, s37, 10, v194
	v_lshl_or_b32 v59, s36, 10, v194
	v_lshl_or_b32 v66, s35, 10, v194
	v_lshl_or_b32 v67, s34, 10, v194
	v_lshl_or_b32 v75, s33, 10, v194
	v_readlane_b32 s28, v231, 11
	v_readlane_b32 s29, v231, 12
	global_load_dwordx4 v[42:45], v50, s[10:11]
	global_load_dwordx4 v[46:49], v51, s[10:11]
	s_nop 0
	global_load_dwordx4 v[50:53], v58, s[10:11]
	global_load_dwordx4 v[54:57], v59, s[10:11]
	s_nop 0
	global_load_dwordx4 v[58:61], v66, s[10:11]
	global_load_dwordx4 v[62:65], v67, s[10:11]
	v_lshl_or_b32 v76, s31, 10, v194
	global_load_dwordx4 v[66:69], v75, s[10:11]
	global_load_dwordx4 v[70:73], v76, s[10:11]
	v_lshl_or_b32 v75, s30, 10, v194
	v_readlane_b32 s25, v231, 9
	v_readlane_b32 s27, v231, 10
	v_lshl_or_b32 v76, s29, 10, v194
	global_load_dwordx4 v[112:115], v75, s[10:11]
	global_load_dwordx4 v[116:119], v76, s[10:11]
	v_lshl_or_b32 v75, s28, 10, v194
	v_readlane_b32 s23, v231, 7
	v_readlane_b32 s24, v231, 8
	v_lshl_or_b32 v76, s27, 10, v194
	global_load_dwordx4 v[144:147], v75, s[10:11]
	global_load_dwordx4 v[148:151], v76, s[10:11]
	v_lshl_or_b32 v75, s25, 10, v194
	v_readlane_b32 s21, v231, 5
	v_readlane_b32 s22, v231, 6
	v_lshl_or_b32 v76, s24, 10, v194
	global_load_dwordx4 v[152:155], v75, s[10:11]
	global_load_dwordx4 v[156:159], v76, s[10:11]
	v_lshl_or_b32 v75, s23, 10, v194
	v_readlane_b32 s19, v231, 3
	v_readlane_b32 s20, v231, 4
	v_lshl_or_b32 v76, s22, 10, v194
	global_load_dwordx4 v[160:163], v75, s[10:11]
	global_load_dwordx4 v[164:167], v76, s[10:11]
	v_lshl_or_b32 v75, s21, 10, v194
	v_readlane_b32 s16, v231, 1
	v_readlane_b32 s18, v231, 2
	v_lshl_or_b32 v76, s20, 10, v194
	global_load_dwordx4 v[168:171], v75, s[10:11]
	global_load_dwordx4 v[172:175], v76, s[10:11]
	v_lshl_or_b32 v75, s19, 10, v194
	v_readlane_b32 s9, v231, 0
	v_lshl_or_b32 v76, s18, 10, v194
	global_load_dwordx4 v[176:179], v75, s[10:11]
	global_load_dwordx4 v[180:183], v76, s[10:11]
	v_lshl_or_b32 v75, s16, 10, v194
	v_lshl_or_b32 v76, s9, 10, v194
	global_load_dwordx4 v[184:187], v75, s[10:11]
	global_load_dwordx4 v[188:191], v76, s[10:11]
	v_and_b32_e32 v75, 1, v0
	v_lshrrev_b32_e32 v76, 2, v0
	v_and_b32_e32 v0, 3, v0
	v_and_or_b32 v193, v76, 12, v0
	v_cmp_eq_u32_e64 s[2:3], 0, v75
	v_mbcnt_lo_u32_b32 v0, -1, 0
	s_mov_b32 s9, 0x800000
	s_mov_b32 s16, 0x45800000
	s_mov_b32 s27, 0x42ee0000
	s_mov_b32 s28, 0x3e6d3388
	s_mov_b32 s29, 0xc040c00
	s_mov_b32 s30, 0xc050c01
	s_mov_b32 s31, 0xc060c02
	s_mov_b32 s33, 0xc070c03
	v_mbcnt_hi_u32_b32 v228, -1, v0
	s_mov_b32 s20, s8
	s_branch .LBB0_1014
; __device__ __forceinline__ void expert_tokens(const unsigned char* __restrict__ UV, const float* __restrict__ US, const float* __restrict__ VS, ...
;     ...
;         float sy = 0.f;
;         const float sumc = wave_sum(sumc_l) * (0.25f / 4096.f);
; #pragma unroll
;         for (int i = 0; i < 16; ++i) { acc[i] = acc[i] * 4096.f - 7.5f * sumc; sy += acc[i] * acc[i]; }
;         const float ry = rsqrtf(wave_sum(sy) * (1.f / 1024.f) + EPS);
.LBB0_1013:
	v_add_f32_dpp v66, v252, v252 quad_perm:[1,0,3,2] row_mask:0xf bank_mask:0xf bound_ctrl:1
	s_ashr_i32 s21, s20, 31
	s_lshl_b64 s[4:5], s[20:21], 12
	v_add_f32_dpp v66, v66, v66 quad_perm:[2,3,0,1] row_mask:0xf bank_mask:0xf bound_ctrl:1
	v_lshl_add_u64 v[162:163], v[200:201], 0, s[4:5]
	s_waitcnt vmcnt(31)
	v_mov_b64_e32 v[190:191], v[80:81]
	v_add_f32_dpp v66, v66, v66 row_ror:4 row_mask:0xf bank_mask:0xf bound_ctrl:1
	s_waitcnt vmcnt(30)
	v_mov_b64_e32 v[186:187], v[76:77]
	s_waitcnt vmcnt(29)
	v_mov_b64_e32 v[182:183], v[88:89]
	v_add_f32_dpp v66, v66, v66 row_ror:8 row_mask:0xf bank_mask:0xf bound_ctrl:1
	v_mov_b32_e32 v67, v66
	s_nop 1
	v_permlane16_swap_b32_e32 v66, v67
	v_add_f32_e32 v66, v66, v67
	v_mov_b32_e32 v67, v66
	s_nop 1
	v_permlane32_swap_b32_e32 v66, v67
	v_add_f32_e32 v66, v66, v67
	v_mul_f32_e32 v66, 0x38800000, v66
	v_mul_f32_e32 v66, 0x40f00000, v66
	v_pk_add_f32 v[224:225], v[224:225], v[220:221] neg_lo:[0,1] neg_hi:[0,1]
	v_pk_add_f32 v[222:223], v[222:223], v[218:219] neg_lo:[0,1] neg_hi:[0,1]
	v_pk_add_f32 v[216:217], v[216:217], v[212:213] neg_lo:[0,1] neg_hi:[0,1]
	v_pk_add_f32 v[214:215], v[214:215], v[210:211] neg_lo:[0,1] neg_hi:[0,1]
	s_mov_b32 s62, 0x43800000
	v_pk_fma_f32 v[118:119], v[224:225], s[16:17], v[66:67] op_sel_hi:[1,0,0] neg_lo:[0,0,1] neg_hi:[0,0,1]
	v_pk_fma_f32 v[144:145], v[222:223], s[16:17], v[66:67] op_sel_hi:[1,0,0] neg_lo:[0,0,1] neg_hi:[0,0,1]
	v_pk_mul_f32 v[68:69], v[118:119], v[118:119]
	v_pk_mul_f32 v[70:71], v[144:145], v[144:145]
	v_add_f32_e32 v68, v68, v69
	v_pk_fma_f32 v[148:149], v[220:221], s[62:63], v[66:67] op_sel_hi:[1,0,0] neg_lo:[0,0,1] neg_hi:[0,0,1]
	v_add_f32_e32 v68, v70, v68
	v_pk_mul_f32 v[72:73], v[148:149], v[148:149]
	v_add_f32_e32 v68, v71, v68
	v_pk_fma_f32 v[150:151], v[218:219], s[62:63], v[66:67] op_sel_hi:[1,0,0] neg_lo:[0,0,1] neg_hi:[0,0,1]
	v_add_f32_e32 v68, v72, v68
	v_pk_mul_f32 v[114:115], v[150:151], v[150:151]
	v_add_f32_e32 v68, v73, v68
	v_pk_fma_f32 v[152:153], v[216:217], s[16:17], v[66:67] op_sel_hi:[1,0,0] neg_lo:[0,0,1] neg_hi:[0,0,1]
	v_add_f32_e32 v68, v114, v68
	v_pk_mul_f32 v[116:117], v[152:153], v[152:153]
	v_add_f32_e32 v68, v115, v68
	v_pk_fma_f32 v[154:155], v[214:215], s[16:17], v[66:67] op_sel_hi:[1,0,0] neg_lo:[0,0,1] neg_hi:[0,0,1]
	v_add_f32_e32 v68, v116, v68
	v_pk_mul_f32 v[146:147], v[154:155], v[154:155]
	v_add_f32_e32 v68, v117, v68
	v_pk_fma_f32 v[156:157], v[212:213], s[62:63], v[66:67] op_sel_hi:[1,0,0] neg_lo:[0,0,1] neg_hi:[0,0,1]
	v_add_f32_e32 v68, v146, v68
	v_pk_mul_f32 v[158:159], v[156:157], v[156:157]
	v_add_f32_e32 v68, v147, v68
	v_pk_fma_f32 v[160:161], v[210:211], s[62:63], v[66:67] op_sel_hi:[1,0,0] neg_lo:[0,0,1] neg_hi:[0,0,1]
	v_add_f32_e32 v68, v158, v68
	v_pk_mul_f32 v[66:67], v[160:161], v[160:161]
	v_add_f32_e32 v68, v159, v68
	v_add_f32_e32 v66, v66, v68
	v_add_f32_e32 v66, v67, v66
	ds_read_b128 v[114:117], v240 offset:8192
	ds_read2st64_b64 v[70:73], v239 offset0:34 offset1:35
	v_add_f32_dpp v66, v66, v66 quad_perm:[1,0,3,2] row_mask:0xf bank_mask:0xf bound_ctrl:1
	s_waitcnt vmcnt(28)
	v_mov_b64_e32 v[178:179], v[84:85]
	s_waitcnt vmcnt(27)
	v_mov_b64_e32 v[174:175], v[96:97]
	v_add_f32_dpp v66, v66, v66 quad_perm:[2,3,0,1] row_mask:0xf bank_mask:0xf bound_ctrl:1
	s_waitcnt vmcnt(26)
; #define LAS __attribute__((address_space(3)))
; __device__ __forceinline__ void expert_tokens(const unsigned char* __restrict__ UV, const float* __restrict__ US, const float* __restrict__ VS, ...
;     ...
;         const float ry = rsqrtf(wave_sum(sy) * (1.f / 1024.f) + EPS);
;         const float pscale = (t < 2048) ? 1.f + pd : 1.f;
; #pragma unroll
;         for (int j = 0; j < 4; ++j) { const f32x4 y = (f32x4){acc[4 * j], acc[4 * j + 1], acc[4 * j + 2], acc[4 * j + 3]};
;             float* op = out + (size_t)t * 1024 + 256 * j + 4 * lane;
;             const u32x2 xw = *(const LAS u32x2*)(xrow + 512 * j + 8 * lane);
;             { const f32x4 ov_ = pscale * (f32x4){__uint_as_float(xw.x << 16), __uint_as_float(xw.x & 0xffff0000u), __uint_as_float(xw.y << 16), __uint_as_float(xw.y & 0xffff0000u)} + pscale * *(const LAS f32x4*)(pvt + 2048 + 256 * j + 4 * lane) * (y * ry); __builtin_nontemporal_store(ov_, (f32x4*)op); } }
;         ci0 = ni0; ci1 = ni1; cg0 = ng0; cg1 = ng1; csu0 = nsu0; csu1 = nsu1; csv0 = nsv0; csv1 = nsv1;
	v_mov_b64_e32 v[170:171], v[92:93]
	v_mov_b64_e32 v[188:189], v[78:79]
	v_add_f32_dpp v66, v66, v66 row_ror:4 row_mask:0xf bank_mask:0xf bound_ctrl:1
	v_mov_b64_e32 v[184:185], v[74:75]
	v_mov_b64_e32 v[180:181], v[86:87]
	v_add_f32_dpp v66, v66, v66 row_ror:8 row_mask:0xf bank_mask:0xf bound_ctrl:1
	v_mov_b32_e32 v67, v66
	s_nop 1
	v_permlane16_swap_b32_e32 v66, v67
	v_add_f32_e32 v66, v66, v67
	v_mov_b32_e32 v67, v66
	s_nop 1
	v_permlane32_swap_b32_e32 v66, v67
	v_add_f32_e32 v66, v66, v67
	v_fmamk_f32 v66, v66, 0x3a800000, v226
	v_mul_f32_e32 v67, 0x4b800000, v66
	v_cmp_gt_f32_e32 vcc, s9, v66
	v_mov_b64_e32 v[176:177], v[82:83]
	v_mov_b64_e32 v[172:173], v[94:95]
	v_cndmask_b32_e32 v66, v66, v67, vcc
	v_rsq_f32_e32 v66, v66
	v_mov_b64_e32 v[168:169], v[90:91]
	v_mov_b32_e32 v231, v242
	s_mov_b64 s[92:93], s[86:87]
	s_mov_b64 s[86:87], s[88:89]
	s_mov_b64 s[88:89], s[92:93]
	v_mov_b32_e32 v232, v243
	v_mul_f32_e32 v67, 0x45800000, v66
	v_cndmask_b32_e32 v158, v66, v67, vcc
	ds_read2st64_b64 v[66:69], v239 offset0:32 offset1:33
	v_pk_mul_f32 v[166:167], v[144:145], v[158:159] op_sel_hi:[1,0]
	ds_read_b128 v[144:147], v240 offset:9216
	v_pk_mul_f32 v[118:119], v[118:119], v[158:159] op_sel_hi:[1,0]
	s_and_b64 vcc, exec, s[18:19]
	s_waitcnt lgkmcnt(1)
	v_lshlrev_b32_e32 v164, 16, v66
	v_and_b32_e32 v165, 0xffff0000, v66
	v_lshlrev_b32_e32 v66, 16, v67
	v_and_b32_e32 v67, 0xffff0000, v67
	v_pk_fma_f32 v[116:117], v[116:117], v[166:167], v[66:67]
	v_pk_fma_f32 v[114:115], v[114:115], v[118:119], v[164:165]
	global_store_dwordx4 v[162:163], v[114:117], off nt
	v_lshlrev_b32_e32 v66, 16, v68
	v_and_b32_e32 v67, 0xffff0000, v68
	v_lshlrev_b32_e32 v68, 16, v69
	v_and_b32_e32 v69, 0xffff0000, v69
	v_pk_mul_f32 v[114:115], v[148:149], v[158:159] op_sel_hi:[1,0]
	v_pk_mul_f32 v[116:117], v[150:151], v[158:159] op_sel_hi:[1,0]
	s_waitcnt lgkmcnt(0)
	v_pk_fma_f32 v[66:67], v[144:145], v[114:115], v[66:67]
	v_pk_fma_f32 v[68:69], v[146:147], v[116:117], v[68:69]
	global_store_dwordx4 v[162:163], v[66:69], off offset:1024 nt
	ds_read_b128 v[66:69], v240 offset:10240
	ds_read_b128 v[114:117], v240 offset:11264
	v_lshlrev_b32_e32 v118, 16, v70
	v_and_b32_e32 v119, 0xffff0000, v70
	v_lshlrev_b32_e32 v70, 16, v71
	v_and_b32_e32 v71, 0xffff0000, v71
	v_pk_mul_f32 v[144:145], v[152:153], v[158:159] op_sel_hi:[1,0]
	v_pk_mul_f32 v[146:147], v[154:155], v[158:159] op_sel_hi:[1,0]
	s_waitcnt lgkmcnt(1)
	v_pk_fma_f32 v[66:67], v[66:67], v[144:145], v[118:119]
	v_pk_fma_f32 v[68:69], v[68:69], v[146:147], v[70:71]
	global_store_dwordx4 v[162:163], v[66:69], off offset:2048 nt
	v_pk_mul_f32 v[70:71], v[156:157], v[158:159] op_sel_hi:[1,0]
	s_waitcnt vmcnt(28)
	v_mov_b64_e32 v[166:167], v[104:105]
	v_lshlrev_b32_e32 v66, 16, v72
	v_and_b32_e32 v67, 0xffff0000, v72
	v_lshlrev_b32_e32 v68, 16, v73
	v_and_b32_e32 v69, 0xffff0000, v73
	v_pk_mul_f32 v[72:73], v[160:161], v[158:159] op_sel_hi:[1,0]
	s_waitcnt lgkmcnt(0)
	v_pk_fma_f32 v[66:67], v[114:115], v[70:71], v[66:67]
	v_pk_fma_f32 v[68:69], v[116:117], v[72:73], v[68:69]
	s_waitcnt vmcnt(26)
	v_mov_b64_e32 v[158:159], v[112:113]
	global_store_dwordx4 v[162:163], v[66:69], off offset:3072 nt
	v_mov_b64_e32 v[162:163], v[100:101]
	v_mov_b64_e32 v[156:157], v[110:111]
	s_waitcnt vmcnt(26)
	v_mov_b64_e32 v[154:155], v[108:109]
	s_waitcnt vmcnt(25)
	v_mov_b64_e32 v[150:151], v[126:127]
	s_waitcnt vmcnt(24)
	v_mov_b64_e32 v[146:147], v[122:123]
	s_waitcnt vmcnt(23)
	v_mov_b64_e32 v[116:117], v[132:133]
	s_waitcnt vmcnt(22)
	v_mov_b64_e32 v[112:113], v[128:129]
	s_waitcnt vmcnt(21)
	v_mov_b64_e32 v[70:71], v[140:141]
	s_waitcnt vmcnt(20)
	v_mov_b64_e32 v[66:67], v[136:137]
	v_mov_b64_e32 v[164:165], v[102:103]
	v_mov_b64_e32 v[160:161], v[98:99]
	v_mov_b64_e32 v[152:153], v[106:107]
	v_mov_b64_e32 v[148:149], v[124:125]
	v_mov_b64_e32 v[144:145], v[120:121]
	v_mov_b64_e32 v[118:119], v[134:135]
	v_mov_b64_e32 v[114:115], v[130:131]
	v_mov_b64_e32 v[72:73], v[142:143]
	v_mov_b64_e32 v[68:69], v[138:139]
	v_mov_b32_e32 v229, v237
	v_mov_b32_e32 v230, v238
	v_mov_b32_e32 v233, v241
	v_mov_b32_e32 v234, v0
	v_mov_b32_e32 v235, v245
	v_mov_b32_e32 v236, v246
	s_mov_b32 s20, s34
	s_cbranch_vccnz .LBB0_1025
.LBB0_1014:
	s_cmp_eq_u32 s84, 0
	s_cbranch_scc1 .Lp10_nobar_t
	s_barrier

.Lp10_nobar_i:
	s_lshl_b32 s92, s21, 2
	s_cmp_lt_u32 s21, 0x80
	s_cselect_b32 s90, s86, s88
	s_cselect_b32 s91, s87, s89
	s_cselect_b32 s92, s92, 0
	s_add_u32 s90, s90, s92
	s_addc_u32 s91, s91, 0
	s_load_dwordx16 s[64:79], s[90:91], 0x0 glc
	v_dot8_i32_i4 v88, v248, v70, 0
	v_dot8_i32_i4 v88, v250, v71, v88
	s_nop 2
	v_lshlrev_b32_e32 v88, 4, v88
	v_dot8_i32_i4 v88, v247, v70, v88
	v_dot8_i32_i4 v74, v248, v188, 0
	v_dot8_i32_i4 v75, v248, v184, 0
	v_dot8_i32_i4 v76, v248, v180, 0
	v_dot8_i32_i4 v77, v248, v176, 0
	v_dot8_i32_i4 v78, v248, v172, 0
	v_dot8_i32_i4 v79, v248, v168, 0
	v_dot8_i32_i4 v80, v248, v164, 0
	v_dot8_i32_i4 v81, v248, v160, 0
	v_dot8_i32_i4 v82, v248, v156, 0
	v_dot8_i32_i4 v83, v248, v152, 0
	v_dot8_i32_i4 v84, v248, v148, 0
	v_dot8_i32_i4 v85, v248, v144, 0
	v_dot8_i32_i4 v86, v248, v116, 0
	v_dot8_i32_i4 v87, v248, v112, 0
	v_dot8_i32_i4 v70, v248, v66, 0
	v_dot8_i32_i4 v74, v250, v189, v74
	v_dot8_i32_i4 v75, v250, v185, v75
	v_dot8_i32_i4 v76, v250, v181, v76
	v_dot8_i32_i4 v77, v250, v177, v77
	v_dot8_i32_i4 v78, v250, v173, v78
	v_dot8_i32_i4 v79, v250, v169, v79
	v_dot8_i32_i4 v80, v250, v165, v80
	v_dot8_i32_i4 v81, v250, v161, v81
	v_dot8_i32_i4 v82, v250, v157, v82
	v_dot8_i32_i4 v83, v250, v153, v83
	v_dot8_i32_i4 v84, v250, v149, v84
	v_dot8_i32_i4 v85, v250, v145, v85
	v_dot8_i32_i4 v86, v250, v117, v86
	v_dot8_i32_i4 v87, v250, v113, v87
	v_dot8_i32_i4 v70, v250, v67, v70
	v_lshlrev_b32_e32 v74, 4, v74
	v_lshlrev_b32_e32 v75, 4, v75
	v_lshlrev_b32_e32 v76, 4, v76
	v_lshlrev_b32_e32 v77, 4, v77
	v_lshlrev_b32_e32 v78, 4, v78
	v_lshlrev_b32_e32 v79, 4, v79
	v_lshlrev_b32_e32 v80, 4, v80
	v_lshlrev_b32_e32 v81, 4, v81
	v_lshlrev_b32_e32 v82, 4, v82
	v_lshlrev_b32_e32 v83, 4, v83
	v_lshlrev_b32_e32 v84, 4, v84
	v_lshlrev_b32_e32 v85, 4, v85
	v_lshlrev_b32_e32 v86, 4, v86
	v_lshlrev_b32_e32 v87, 4, v87
	v_lshlrev_b32_e32 v70, 4, v70
	v_dot8_i32_i4 v74, v247, v188, v74
	v_dot8_i32_i4 v75, v247, v184, v75
	v_dot8_i32_i4 v76, v247, v180, v76
	v_dot8_i32_i4 v77, v247, v176, v77
	v_dot8_i32_i4 v78, v247, v172, v78
	v_dot8_i32_i4 v79, v247, v168, v79
	v_dot8_i32_i4 v80, v247, v164, v80
	v_dot8_i32_i4 v81, v247, v160, v81
	v_dot8_i32_i4 v82, v247, v156, v82
	v_dot8_i32_i4 v83, v247, v152, v83
	v_dot8_i32_i4 v84, v247, v148, v84
	v_dot8_i32_i4 v85, v247, v144, v85
	v_dot8_i32_i4 v86, v247, v116, v86
	v_dot8_i32_i4 v87, v247, v112, v87
	v_dot8_i32_i4 v70, v247, v66, v70
	v_dot8_i32_i4 v74, v249, v189, v74
	v_dot8_i32_i4 v75, v249, v185, v75
	v_dot8_i32_i4 v76, v249, v181, v76
	v_dot8_i32_i4 v77, v249, v177, v77
	v_dot8_i32_i4 v78, v249, v173, v78
	v_dot8_i32_i4 v79, v249, v169, v79
	v_dot8_i32_i4 v80, v249, v165, v80
	v_dot8_i32_i4 v81, v249, v161, v81
	v_dot8_i32_i4 v82, v249, v157, v82
	v_dot8_i32_i4 v83, v249, v153, v83
	v_dot8_i32_i4 v84, v249, v149, v84
	v_dot8_i32_i4 v85, v249, v145, v85
	v_dot8_i32_i4 v86, v249, v117, v86
	v_dot8_i32_i4 v87, v249, v113, v87
	v_dot8_i32_i4 v88, v249, v71, v88
	v_dot8_i32_i4 v70, v249, v67, v70
	v_permlane32_swap_b32_e32 v74, v82
	v_permlane32_swap_b32_e32 v75, v83
	v_permlane32_swap_b32_e32 v76, v84
	v_permlane32_swap_b32_e32 v77, v85
	v_permlane32_swap_b32_e32 v78, v86
	v_permlane32_swap_b32_e32 v79, v87
	v_permlane32_swap_b32_e32 v80, v88
	v_permlane32_swap_b32_e32 v81, v70
	v_add_u32_e32 v66, v74, v82
	v_add_u32_e32 v67, v75, v83
	v_add_u32_e32 v71, v76, v84
	v_add_u32_e32 v74, v77, v85
	v_add_u32_e32 v75, v78, v86
	v_add_u32_e32 v76, v79, v87
	v_add_u32_e32 v77, v80, v88
	v_add_u32_e32 v70, v81, v70
	v_permlane16_swap_b32_e32 v66, v75
	v_permlane16_swap_b32_e32 v67, v76
	v_permlane16_swap_b32_e32 v71, v77
	v_permlane16_swap_b32_e32 v74, v70
	v_add_u32_e32 v66, v66, v75
	v_add_u32_e32 v67, v67, v76
	v_add_u32_e32 v71, v71, v77
	v_add_u32_e32 v70, v74, v70
	v_cndmask_b32_e64 v74, v71, v66, s[0:1]
	v_cndmask_b32_e64 v66, v66, v71, s[0:1]
	v_cndmask_b32_e64 v71, v70, v67, s[0:1]
	v_cndmask_b32_e64 v67, v67, v70, s[0:1]
	v_add_u32_dpp v66, v66, v74 quad_perm:[2,3,0,1] row_mask:0xf bank_mask:0xf bound_ctrl:1
	s_sub_i32 s4, s21, 32
	v_add_u32_dpp v67, v67, v71 quad_perm:[2,3,0,1] row_mask:0xf bank_mask:0xf bound_ctrl:1
	v_cndmask_b32_e64 v70, v67, v66, s[2:3]
	v_cndmask_b32_e64 v66, v66, v67, s[2:3]
	s_cmp_lt_u32 s25, 4
	s_cselect_b64 vcc, -1, 0
	v_add_u32_dpp v66, v66, v70 quad_perm:[1,0,3,2] row_mask:0xf bank_mask:0xf bound_ctrl:1
	v_cndmask_b32_e32 v70, v234, v233, vcc
	v_cndmask_b32_e32 v71, v230, v229, vcc
	v_add_u32_dpp v66, v66, v66 row_ror:8 row_mask:0xf bank_mask:0xf bound_ctrl:1
	s_cmp_eq_u32 s21, 32
	s_nop 0
	v_add_u32_dpp v67, v66, v66 row_ror:4 row_mask:0xf bank_mask:0xf bound_ctrl:1
	v_and_or_b32 v66, s4, 32, v193
	v_lshlrev_b32_e32 v66, 2, v66
	v_cvt_f32_i32_e32 v74, v67
	s_waitcnt lgkmcnt(0)
	ds_bpermute_b32 v75, v66, v70
	v_and_b32_e32 v67, 0xffff0000, v71
	ds_bpermute_b32 v76, v66, v67
	v_add_f32_e32 v71, v251, v74
	v_mul_f32_e32 v71, v244, v71
	s_waitcnt lgkmcnt(1)
	v_mul_f32_e32 v74, v71, v75
	v_fma_f32 v71, |v74|, s28, 1.0
	v_rcp_f32_e32 v75, v71
	v_mul_f32_e32 v79, v74, v74
	v_mul_f32_e32 v79, 0xbf38aa3b, v79
	v_exp_f32_e32 v79, v79
	v_fmamk_f32 v78, v75, 0x3f07dc22, v227
	v_fmaak_f32 v78, v75, v78, 0x3f35f0e3
	v_fmaak_f32 v78, v75, v78, 0xbe11a98e
	v_cndmask_b32_e32 v71, v236, v235, vcc
	v_fmaak_f32 v78, v75, v78, 0x3e027906
	ds_bpermute_b32 v77, v66, v71
	v_mul_f32_e32 v75, v75, v78
	v_mul_f32_e32 v75, v79, v75
	v_mul_f32_e32 v78, v74, v75
	v_fma_f32 v75, -v74, v75, v74
	v_cmp_gt_f32_e32 vcc, 0, v74
	s_nop 1
	v_cndmask_b32_e32 v74, v75, v78, vcc
	s_waitcnt lgkmcnt(1)
	v_mul_f32_e32 v74, v74, v76
	s_cselect_b64 vcc, -1, 0
	s_cmp_gt_u32 s25, 5
	s_waitcnt lgkmcnt(0)
	v_mul_f32_e32 v74, v74, v77
	s_cselect_b64 s[22:23], -1, 0
	s_cmp_lt_u32 s25, 6
	v_fma_mixlo_f16 v116, v74, s16, 0
	s_cselect_b64 s[4:5], -1, 0
	v_and_b32_e32 v117, 0xffff, v116
	s_nop 1
	v_mov_b32_dpp v207, v117 quad_perm:[1,0,3,2] row_mask:0xf bank_mask:0xf
	s_cmp_lg_u32 s21, 32
	v_lshl_or_b32 v209, v207, 16, v117
	s_nop 0
	v_readlane_b32 s47, v209, 0
	v_readlane_b32 s45, v209, 2
	v_readlane_b32 s43, v209, 16
	v_readlane_b32 s41, v209, 18
	v_readlane_b32 s39, v209, 32
	v_readlane_b32 s37, v209, 34
	v_readlane_b32 s35, v209, 48
	v_readlane_b32 s4, v209, 50
	buffer_load_dwordx4 v[78:81], v194, s[80:83], s64 offen
	buffer_load_dwordx4 v[74:77], v194, s[80:83], s65 offen
	buffer_load_dwordx4 v[86:89], v194, s[80:83], s66 offen
	buffer_load_dwordx4 v[82:85], v194, s[80:83], s67 offen
	buffer_load_dwordx4 v[94:97], v194, s[80:83], s68 offen
	buffer_load_dwordx4 v[90:93], v194, s[80:83], s69 offen
	buffer_load_dwordx4 v[102:105], v194, s[80:83], s70 offen
	buffer_load_dwordx4 v[98:101], v194, s[80:83], s71 offen
	buffer_load_dwordx4 v[110:113], v194, s[80:83], s72 offen
	buffer_load_dwordx4 v[106:109], v194, s[80:83], s73 offen
	buffer_load_dwordx4 v[124:127], v194, s[80:83], s74 offen
	buffer_load_dwordx4 v[120:123], v194, s[80:83], s75 offen
	buffer_load_dwordx4 v[132:135], v194, s[80:83], s76 offen
	buffer_load_dwordx4 v[128:131], v194, s[80:83], s77 offen
	buffer_load_dwordx4 v[140:143], v194, s[80:83], s78 offen
	buffer_load_dwordx4 v[136:139], v194, s[80:83], s79 offen
	s_cbranch_scc1 .LBB0_1021
	s_waitcnt vmcnt(16)
	s_bfe_i32 s60, s34, 0x10000
	v_alignbit_b32 v237, v237, v237, 16
	v_alignbit_b32 v238, v238, v238, 16
	v_xor_b32_e32 v237, s60, v237
	v_xor_b32_e32 v238, s60, v238
	s_nop 1
	s_mov_b32 s58, 0x99999999
	s_mov_b32 s59, 0x99999999
	v_min_u32_dpp v202, v237, v237 quad_perm:[1,0,3,2] row_mask:0xf bank_mask:0xf
	v_max_u32_dpp v203, v237, v237 quad_perm:[1,0,3,2] row_mask:0xf bank_mask:0xf
	v_min_u32_dpp v204, v238, v238 quad_perm:[1,0,3,2] row_mask:0xf bank_mask:0xf
	v_max_u32_dpp v205, v238, v238 quad_perm:[1,0,3,2] row_mask:0xf bank_mask:0xf
	v_cndmask_b32_e64 v237, v203, v202, s[58:59]
	v_cndmask_b32_e64 v238, v205, v204, s[58:59]
	s_mov_b32 s58, 0xcc33cc33
	s_mov_b32 s59, 0xcc33cc33
	v_min_u32_dpp v202, v237, v237 quad_perm:[2,3,0,1] row_mask:0xf bank_mask:0xf
	v_max_u32_dpp v203, v237, v237 quad_perm:[2,3,0,1] row_mask:0xf bank_mask:0xf
	v_min_u32_dpp v204, v238, v238 quad_perm:[2,3,0,1] row_mask:0xf bank_mask:0xf
	v_max_u32_dpp v205, v238, v238 quad_perm:[2,3,0,1] row_mask:0xf bank_mask:0xf
	v_cndmask_b32_e64 v237, v203, v202, s[58:59]
	v_cndmask_b32_e64 v238, v205, v204, s[58:59]
	s_mov_b32 s58, 0xaa55aa55
	s_mov_b32 s59, 0xaa55aa55
	v_min_u32_dpp v202, v237, v237 quad_perm:[1,0,3,2] row_mask:0xf bank_mask:0xf
	v_max_u32_dpp v203, v237, v237 quad_perm:[1,0,3,2] row_mask:0xf bank_mask:0xf
	v_min_u32_dpp v204, v238, v238 quad_perm:[1,0,3,2] row_mask:0xf bank_mask:0xf
	v_max_u32_dpp v205, v238, v238 quad_perm:[1,0,3,2] row_mask:0xf bank_mask:0xf
	v_cndmask_b32_e64 v237, v203, v202, s[58:59]
	v_cndmask_b32_e64 v238, v205, v204, s[58:59]
	s_mov_b32 s58, 0xf00ff00f
	s_mov_b32 s59, 0xf00ff00f
	v_min_u32_dpp v202, v237, v237 row_ror:8 row_mask:0xf bank_mask:0xf
	v_max_u32_dpp v203, v237, v237 row_ror:8 row_mask:0xf bank_mask:0xf
	v_min_u32_dpp v204, v238, v238 row_ror:8 row_mask:0xf bank_mask:0xf
	v_max_u32_dpp v205, v238, v238 row_ror:8 row_mask:0xf bank_mask:0xf
	v_cndmask_b32_e64 v237, v203, v202, s[58:59]
	v_cndmask_b32_e64 v238, v205, v204, s[58:59]
	s_mov_b32 s58, 0xc3c3c3c3
	s_mov_b32 s59, 0xc3c3c3c3
	v_min_u32_dpp v202, v237, v237 quad_perm:[2,3,0,1] row_mask:0xf bank_mask:0xf
	v_max_u32_dpp v203, v237, v237 quad_perm:[2,3,0,1] row_mask:0xf bank_mask:0xf
	v_min_u32_dpp v204, v238, v238 quad_perm:[2,3,0,1] row_mask:0xf bank_mask:0xf
	v_max_u32_dpp v205, v238, v238 quad_perm:[2,3,0,1] row_mask:0xf bank_mask:0xf
	v_cndmask_b32_e64 v237, v203, v202, s[58:59]
	v_cndmask_b32_e64 v238, v205, v204, s[58:59]
	s_mov_b32 s58, 0xa5a5a5a5
	s_mov_b32 s59, 0xa5a5a5a5
	v_min_u32_dpp v202, v237, v237 quad_perm:[1,0,3,2] row_mask:0xf bank_mask:0xf
	v_max_u32_dpp v203, v237, v237 quad_perm:[1,0,3,2] row_mask:0xf bank_mask:0xf
	v_min_u32_dpp v204, v238, v238 quad_perm:[1,0,3,2] row_mask:0xf bank_mask:0xf
	v_max_u32_dpp v205, v238, v238 quad_perm:[1,0,3,2] row_mask:0xf bank_mask:0xf
	v_cndmask_b32_e64 v237, v203, v202, s[58:59]
	v_cndmask_b32_e64 v238, v205, v204, s[58:59]
	s_mov_b32 s58, 0xf0f00f0f
	s_mov_b32 s59, 0xf0f00f0f
	v_mov_b32_dpp v202, v237 row_half_mirror row_mask:0xf bank_mask:0xf
	v_mov_b32_dpp v204, v238 row_half_mirror row_mask:0xf bank_mask:0xf
	s_nop 0
	v_max_u32_dpp v203, v202, v237 quad_perm:[3,2,1,0] row_mask:0xf bank_mask:0xf
	v_max_u32_dpp v205, v204, v238 quad_perm:[3,2,1,0] row_mask:0xf bank_mask:0xf
	v_min_u32_dpp v202, v202, v237 quad_perm:[3,2,1,0] row_mask:0xf bank_mask:0xf
	v_min_u32_dpp v204, v204, v238 quad_perm:[3,2,1,0] row_mask:0xf bank_mask:0xf
	v_cndmask_b32_e64 v237, v203, v202, s[58:59]
	v_cndmask_b32_e64 v238, v205, v204, s[58:59]
	s_mov_b32 s58, 0xff0000ff
	s_mov_b32 s59, 0xff0000ff
	v_min_u32_dpp v202, v237, v237 row_ror:8 row_mask:0xf bank_mask:0xf
	v_max_u32_dpp v203, v237, v237 row_ror:8 row_mask:0xf bank_mask:0xf
	v_min_u32_dpp v204, v238, v238 row_ror:8 row_mask:0xf bank_mask:0xf
	v_max_u32_dpp v205, v238, v238 row_ror:8 row_mask:0xf bank_mask:0xf
	v_cndmask_b32_e64 v237, v203, v202, s[58:59]
	v_cndmask_b32_e64 v238, v205, v204, s[58:59]
	s_mov_b32 s58, 0xcccc3333
	s_mov_b32 s59, 0xcccc3333
	v_min_u32_dpp v202, v237, v237 quad_perm:[2,3,0,1] row_mask:0xf bank_mask:0xf
; __device__ __forceinline__ void expert_tokens(const unsigned char* __restrict__ UV, const float* __restrict__ US, const float* __restrict__ VS, ...
;     ...
;         const unsigned nw0 = (unsigned)IDX[(size_t)tn * 128 + lane], nw1 = (unsigned)IDX[(size_t)tn * 128 + 64 + lane];
;         const int ni0 = (int)nw0 & rmask, ni1 = (int)nw1 & rmask;
;         const float ng0 = __uint_as_float(nw0 & 0xFFFF0000u), ng1 = __uint_as_float(nw1 & 0xFFFF0000u);
;     ...
;             if (bi == 0) { nsu0 = US[ni0]; nsu1 = US[ni1]; nsv0 = VS[ni0]; nsv1 = VS[ni1]; }
	v_max_u32_dpp v203, v237, v237 quad_perm:[2,3,0,1] row_mask:0xf bank_mask:0xf
	v_min_u32_dpp v204, v238, v238 quad_perm:[2,3,0,1] row_mask:0xf bank_mask:0xf
	v_max_u32_dpp v205, v238, v238 quad_perm:[2,3,0,1] row_mask:0xf bank_mask:0xf
	v_cndmask_b32_e64 v237, v203, v202, s[58:59]
	v_cndmask_b32_e64 v238, v205, v204, s[58:59]
	s_mov_b32 s58, 0xaaaa5555
	s_mov_b32 s59, 0xaaaa5555
	v_min_u32_dpp v202, v237, v237 quad_perm:[1,0,3,2] row_mask:0xf bank_mask:0xf
	v_max_u32_dpp v203, v237, v237 quad_perm:[1,0,3,2] row_mask:0xf bank_mask:0xf
	v_min_u32_dpp v204, v238, v238 quad_perm:[1,0,3,2] row_mask:0xf bank_mask:0xf
	v_max_u32_dpp v205, v238, v238 quad_perm:[1,0,3,2] row_mask:0xf bank_mask:0xf
	v_cndmask_b32_e64 v237, v203, v202, s[58:59]
	v_cndmask_b32_e64 v238, v205, v204, s[58:59]
	s_nop 1
	v_permlane16_swap_b32_e32 v237, v238
	s_mov_b32 s58, -1
	s_mov_b32 s59, 0
	v_min_u32_e32 v202, v237, v238
	v_max_u32_e32 v203, v237, v238
	v_cndmask_b32_e64 v237, v203, v202, s[58:59]
	v_cndmask_b32_e64 v238, v202, v203, s[58:59]
	s_mov_b32 s58, 0xf0f0f0f
	s_mov_b32 s59, 0xf0f0f0f0
	v_mov_b32_dpp v202, v237 row_half_mirror row_mask:0xf bank_mask:0xf
	v_mov_b32_dpp v204, v238 row_half_mirror row_mask:0xf bank_mask:0xf
	s_nop 0
	v_max_u32_dpp v203, v202, v237 quad_perm:[3,2,1,0] row_mask:0xf bank_mask:0xf
	v_max_u32_dpp v205, v204, v238 quad_perm:[3,2,1,0] row_mask:0xf bank_mask:0xf
	v_min_u32_dpp v202, v202, v237 quad_perm:[3,2,1,0] row_mask:0xf bank_mask:0xf
	v_min_u32_dpp v204, v204, v238 quad_perm:[3,2,1,0] row_mask:0xf bank_mask:0xf
	v_cndmask_b32_e64 v237, v203, v202, s[58:59]
	v_cndmask_b32_e64 v238, v205, v204, s[58:59]
	s_mov_b32 s58, 0xff00ff
	s_mov_b32 s59, 0xff00ff00
	v_min_u32_dpp v202, v237, v237 row_ror:8 row_mask:0xf bank_mask:0xf
	v_max_u32_dpp v203, v237, v237 row_ror:8 row_mask:0xf bank_mask:0xf
	v_min_u32_dpp v204, v238, v238 row_ror:8 row_mask:0xf bank_mask:0xf
	v_max_u32_dpp v205, v238, v238 row_ror:8 row_mask:0xf bank_mask:0xf
	v_cndmask_b32_e64 v237, v203, v202, s[58:59]
	v_cndmask_b32_e64 v238, v205, v204, s[58:59]
	s_mov_b32 s58, 0x33333333
	s_mov_b32 s59, 0xcccccccc
	v_min_u32_dpp v202, v237, v237 quad_perm:[2,3,0,1] row_mask:0xf bank_mask:0xf
	v_max_u32_dpp v203, v237, v237 quad_perm:[2,3,0,1] row_mask:0xf bank_mask:0xf
	v_min_u32_dpp v204, v238, v238 quad_perm:[2,3,0,1] row_mask:0xf bank_mask:0xf
	v_max_u32_dpp v205, v238, v238 quad_perm:[2,3,0,1] row_mask:0xf bank_mask:0xf
	v_cndmask_b32_e64 v237, v203, v202, s[58:59]
	v_cndmask_b32_e64 v238, v205, v204, s[58:59]
	s_mov_b32 s58, 0x55555555
	s_mov_b32 s59, 0xaaaaaaaa
	v_min_u32_dpp v202, v237, v237 quad_perm:[1,0,3,2] row_mask:0xf bank_mask:0xf
	v_max_u32_dpp v203, v237, v237 quad_perm:[1,0,3,2] row_mask:0xf bank_mask:0xf
	v_min_u32_dpp v204, v238, v238 quad_perm:[1,0,3,2] row_mask:0xf bank_mask:0xf
	v_max_u32_dpp v205, v238, v238 quad_perm:[1,0,3,2] row_mask:0xf bank_mask:0xf
	v_cndmask_b32_e64 v237, v203, v202, s[58:59]
	v_cndmask_b32_e64 v238, v205, v204, s[58:59]
	s_nop 1
	v_permlane32_swap_b32_e32 v237, v238
	s_mov_b32 s58, 0xffff
	s_mov_b32 s59, 0xffff
	v_min_u32_e32 v202, v237, v238
	v_max_u32_e32 v203, v237, v238
	v_cndmask_b32_e64 v237, v203, v202, s[58:59]
	v_cndmask_b32_e64 v238, v202, v203, s[58:59]
	s_nop 1
	v_permlane32_swap_b32_e32 v237, v238
	s_mov_b32 s58, 0xffff
	s_mov_b32 s59, 0xffff
	v_min_u32_e32 v202, v237, v238
	v_max_u32_e32 v203, v237, v238
	v_cndmask_b32_e64 v237, v203, v202, s[58:59]
	v_cndmask_b32_e64 v238, v202, v203, s[58:59]
	s_mov_b32 s58, 0xf0f00f0f
	s_mov_b32 s59, 0xf0f00f0f
	v_mov_b32_dpp v202, v237 row_half_mirror row_mask:0xf bank_mask:0xf
	v_mov_b32_dpp v204, v238 row_half_mirror row_mask:0xf bank_mask:0xf
	s_nop 0
	v_max_u32_dpp v203, v202, v237 quad_perm:[3,2,1,0] row_mask:0xf bank_mask:0xf
	v_max_u32_dpp v205, v204, v238 quad_perm:[3,2,1,0] row_mask:0xf bank_mask:0xf
	v_min_u32_dpp v202, v202, v237 quad_perm:[3,2,1,0] row_mask:0xf bank_mask:0xf
	v_min_u32_dpp v204, v204, v238 quad_perm:[3,2,1,0] row_mask:0xf bank_mask:0xf
	v_cndmask_b32_e64 v237, v203, v202, s[58:59]
	v_cndmask_b32_e64 v238, v205, v204, s[58:59]
	s_mov_b32 s58, 0xff0000ff
	s_mov_b32 s59, 0xff0000ff
	v_min_u32_dpp v202, v237, v237 row_ror:8 row_mask:0xf bank_mask:0xf
	v_max_u32_dpp v203, v237, v237 row_ror:8 row_mask:0xf bank_mask:0xf
	v_min_u32_dpp v204, v238, v238 row_ror:8 row_mask:0xf bank_mask:0xf
	v_max_u32_dpp v205, v238, v238 row_ror:8 row_mask:0xf bank_mask:0xf
	v_cndmask_b32_e64 v237, v203, v202, s[58:59]
	v_cndmask_b32_e64 v238, v205, v204, s[58:59]
	s_mov_b32 s58, 0xcccc3333
	s_mov_b32 s59, 0xcccc3333
	v_min_u32_dpp v202, v237, v237 quad_perm:[2,3,0,1] row_mask:0xf bank_mask:0xf
	v_max_u32_dpp v203, v237, v237 quad_perm:[2,3,0,1] row_mask:0xf bank_mask:0xf
	v_min_u32_dpp v204, v238, v238 quad_perm:[2,3,0,1] row_mask:0xf bank_mask:0xf
	v_max_u32_dpp v205, v238, v238 quad_perm:[2,3,0,1] row_mask:0xf bank_mask:0xf
	v_cndmask_b32_e64 v237, v203, v202, s[58:59]
	v_cndmask_b32_e64 v238, v205, v204, s[58:59]
	s_mov_b32 s58, 0xaaaa5555
	s_mov_b32 s59, 0xaaaa5555
	v_min_u32_dpp v202, v237, v237 quad_perm:[1,0,3,2] row_mask:0xf bank_mask:0xf
	v_max_u32_dpp v203, v237, v237 quad_perm:[1,0,3,2] row_mask:0xf bank_mask:0xf
	v_min_u32_dpp v204, v238, v238 quad_perm:[1,0,3,2] row_mask:0xf bank_mask:0xf
	v_max_u32_dpp v205, v238, v238 quad_perm:[1,0,3,2] row_mask:0xf bank_mask:0xf
	v_cndmask_b32_e64 v237, v203, v202, s[58:59]
	v_cndmask_b32_e64 v238, v205, v204, s[58:59]
	s_nop 1
	v_permlane16_swap_b32_e32 v237, v238
	v_min_u32_e32 v202, v237, v238
	v_max_u32_e32 v238, v237, v238
	v_mov_b32_e32 v237, v202
	s_nop 1
	v_permlane32_swap_b32_e32 v237, v238
	v_min_u32_e32 v202, v237, v238
	v_max_u32_e32 v238, v237, v238
	v_mov_b32_e32 v237, v202
	s_nop 1
	v_permlane16_swap_b32_e32 v237, v238
	v_min_u32_e32 v202, v237, v238
	v_max_u32_e32 v238, v237, v238
	v_mov_b32_e32 v237, v202
	s_nop 1
	v_permlane16_swap_b32_e32 v237, v238
	s_nop 1
	v_permlane32_swap_b32_e32 v237, v238
	v_xor_b32_e32 v237, s60, v237
	v_xor_b32_e32 v238, s60, v238
	v_alignbit_b32 v237, v237, v237, 16
	v_alignbit_b32 v238, v238, v238, 16
	v_and_b32_e32 v242, 0x3fff, v237
	v_and_b32_e32 v243, 0x3fff, v238
	v_lshlrev_b32_e32 v208, 2, v242
	v_lshlrev_b32_e32 v206, 2, v243
	v_lshlrev_b32_e32 v204, 10, v242
	v_lshlrev_b32_e32 v205, 10, v243
	global_store_dword v192, v204, s[88:89]
	global_store_dword v192, v205, s[88:89] offset:256
	global_load_dword v241, v208, s[12:13]
	global_load_dword v0, v206, s[12:13]
	global_load_dword v245, v208, s[14:15]
	global_load_dword v246, v206, s[14:15]
.LBB0_1021:
	s_lshl_b32 s92, s21, 2
	s_cmp_lt_u32 s21, 0x80
	s_cselect_b32 s90, s86, s88
	s_cselect_b32 s91, s87, s89
	s_cselect_b32 s92, s92, 0
	s_add_u32 s90, s90, s92
	s_addc_u32 s91, s91, 0
	s_load_dwordx16 s[64:79], s[90:91], 0x40 glc
	v_perm_b32 v149, v186, v190, s29
	v_dot2c_f32_f16_e32 v224, s47, v149
	v_and_b32_e32 v149, s32, v149
	v_dot2c_f32_f16_e32 v220, s47, v149
	v_perm_b32 v149, v186, v190, s30
	v_dot2c_f32_f16_e32 v225, s47, v149
	v_and_b32_e32 v149, s32, v149
	v_dot2c_f32_f16_e32 v221, s47, v149
	v_perm_b32 v149, v186, v190, s31
	v_perm_b32 v117, v186, v190, s33
	v_dot2c_f32_f16_e32 v223, s47, v117
	v_and_b32_e32 v117, s32, v117
	v_dot2c_f32_f16_e32 v222, s47, v149
	v_and_b32_e32 v149, s32, v149
	v_dot2c_f32_f16_e32 v219, s47, v117
	v_dot2c_f32_f16_e32 v218, s47, v149
	v_perm_b32 v149, v187, v191, s29
	v_dot2c_f32_f16_e32 v216, s47, v149
	v_and_b32_e32 v149, s32, v149
	v_dot2c_f32_f16_e32 v212, s47, v149
	v_perm_b32 v149, v187, v191, s30
	v_dot2c_f32_f16_e32 v217, s47, v149
	v_and_b32_e32 v149, s32, v149
	v_dot2c_f32_f16_e32 v213, s47, v149
	v_perm_b32 v149, v187, v191, s31
	v_perm_b32 v117, v187, v191, s33
	v_dot2c_f32_f16_e32 v215, s47, v117
	v_and_b32_e32 v117, s32, v117
	v_dot2c_f32_f16_e32 v214, s47, v149
	v_and_b32_e32 v149, s32, v149
	v_dot2c_f32_f16_e32 v211, s47, v117
	v_dot2c_f32_f16_e32 v210, s47, v149
	v_perm_b32 v149, v178, v182, s29
	v_dot2c_f32_f16_e32 v224, s45, v149
	v_and_b32_e32 v149, s32, v149
	v_dot2c_f32_f16_e32 v220, s45, v149
	v_perm_b32 v149, v178, v182, s30
	v_dot2c_f32_f16_e32 v225, s45, v149
	v_and_b32_e32 v149, s32, v149
	v_dot2c_f32_f16_e32 v221, s45, v149
	v_perm_b32 v149, v178, v182, s31
	v_perm_b32 v117, v178, v182, s33
	v_dot2c_f32_f16_e32 v223, s45, v117
	v_and_b32_e32 v117, s32, v117
	v_dot2c_f32_f16_e32 v222, s45, v149
	v_and_b32_e32 v149, s32, v149
	v_dot2c_f32_f16_e32 v219, s45, v117
	v_dot2c_f32_f16_e32 v218, s45, v149
	v_perm_b32 v149, v179, v183, s29
	v_dot2c_f32_f16_e32 v216, s45, v149
	v_and_b32_e32 v149, s32, v149
	v_dot2c_f32_f16_e32 v212, s45, v149
	v_perm_b32 v149, v179, v183, s30
	v_dot2c_f32_f16_e32 v217, s45, v149
	v_and_b32_e32 v149, s32, v149
	v_dot2c_f32_f16_e32 v213, s45, v149
	v_perm_b32 v149, v179, v183, s31
	v_perm_b32 v117, v179, v183, s33
	v_dot2c_f32_f16_e32 v215, s45, v117
	v_and_b32_e32 v117, s32, v117
	v_dot2c_f32_f16_e32 v214, s45, v149
	v_and_b32_e32 v149, s32, v149
	v_dot2c_f32_f16_e32 v211, s45, v117
	v_dot2c_f32_f16_e32 v210, s45, v149
	v_perm_b32 v149, v170, v174, s29
	v_dot2c_f32_f16_e32 v224, s43, v149
	v_and_b32_e32 v149, s32, v149
	v_dot2c_f32_f16_e32 v220, s43, v149
	v_perm_b32 v149, v170, v174, s30
	v_dot2c_f32_f16_e32 v225, s43, v149
	v_and_b32_e32 v149, s32, v149
	v_dot2c_f32_f16_e32 v221, s43, v149
	v_perm_b32 v149, v170, v174, s31
	v_perm_b32 v117, v170, v174, s33
	v_dot2c_f32_f16_e32 v223, s43, v117
	v_and_b32_e32 v117, s32, v117
	v_dot2c_f32_f16_e32 v222, s43, v149
	v_and_b32_e32 v149, s32, v149
	v_dot2c_f32_f16_e32 v219, s43, v117
	v_dot2c_f32_f16_e32 v218, s43, v149
	v_perm_b32 v149, v171, v175, s29
	v_dot2c_f32_f16_e32 v216, s43, v149
	v_and_b32_e32 v149, s32, v149
	v_dot2c_f32_f16_e32 v212, s43, v149
	v_perm_b32 v149, v171, v175, s30
	v_dot2c_f32_f16_e32 v217, s43, v149
	v_and_b32_e32 v149, s32, v149
	v_dot2c_f32_f16_e32 v213, s43, v149
	v_perm_b32 v149, v171, v175, s31
	v_perm_b32 v117, v171, v175, s33
	v_dot2c_f32_f16_e32 v215, s43, v117
	v_and_b32_e32 v117, s32, v117
	v_dot2c_f32_f16_e32 v214, s43, v149
	v_and_b32_e32 v149, s32, v149
	v_dot2c_f32_f16_e32 v211, s43, v117
	v_dot2c_f32_f16_e32 v210, s43, v149
	v_perm_b32 v149, v162, v166, s29
	v_dot2c_f32_f16_e32 v224, s41, v149
	v_and_b32_e32 v149, s32, v149
	v_dot2c_f32_f16_e32 v220, s41, v149
	v_perm_b32 v149, v162, v166, s30
	v_dot2c_f32_f16_e32 v225, s41, v149
	v_and_b32_e32 v149, s32, v149
	v_dot2c_f32_f16_e32 v221, s41, v149
	v_perm_b32 v149, v162, v166, s31
	v_perm_b32 v117, v162, v166, s33
	v_dot2c_f32_f16_e32 v223, s41, v117
	v_and_b32_e32 v117, s32, v117
	v_dot2c_f32_f16_e32 v222, s41, v149
	v_and_b32_e32 v149, s32, v149
	v_dot2c_f32_f16_e32 v219, s41, v117
	v_dot2c_f32_f16_e32 v218, s41, v149
	v_perm_b32 v149, v163, v167, s29
	v_dot2c_f32_f16_e32 v216, s41, v149
	v_and_b32_e32 v149, s32, v149
	v_dot2c_f32_f16_e32 v212, s41, v149
	v_perm_b32 v149, v163, v167, s30
	v_dot2c_f32_f16_e32 v217, s41, v149
	v_and_b32_e32 v149, s32, v149
	v_dot2c_f32_f16_e32 v213, s41, v149
	v_perm_b32 v149, v163, v167, s31
	v_perm_b32 v117, v163, v167, s33
	v_dot2c_f32_f16_e32 v215, s41, v117
	v_and_b32_e32 v117, s32, v117
	v_dot2c_f32_f16_e32 v214, s41, v149
	v_and_b32_e32 v149, s32, v149
	v_dot2c_f32_f16_e32 v211, s41, v117
	v_dot2c_f32_f16_e32 v210, s41, v149
	v_perm_b32 v149, v154, v158, s29
	v_dot2c_f32_f16_e32 v224, s39, v149
	v_and_b32_e32 v149, s32, v149
	v_dot2c_f32_f16_e32 v220, s39, v149
	v_perm_b32 v149, v154, v158, s30
	v_dot2c_f32_f16_e32 v225, s39, v149
	v_and_b32_e32 v149, s32, v149
	v_dot2c_f32_f16_e32 v221, s39, v149
	v_perm_b32 v149, v154, v158, s31
	v_perm_b32 v117, v154, v158, s33
	v_dot2c_f32_f16_e32 v223, s39, v117
	v_and_b32_e32 v117, s32, v117
	v_dot2c_f32_f16_e32 v222, s39, v149
	v_and_b32_e32 v149, s32, v149
	v_dot2c_f32_f16_e32 v219, s39, v117
	v_dot2c_f32_f16_e32 v218, s39, v149
	v_perm_b32 v149, v155, v159, s29
	v_dot2c_f32_f16_e32 v216, s39, v149
	v_and_b32_e32 v149, s32, v149
	v_dot2c_f32_f16_e32 v212, s39, v149
	v_perm_b32 v149, v155, v159, s30
	v_dot2c_f32_f16_e32 v217, s39, v149
	v_and_b32_e32 v149, s32, v149
	v_dot2c_f32_f16_e32 v213, s39, v149
	v_perm_b32 v149, v155, v159, s31
	v_perm_b32 v117, v155, v159, s33
	v_dot2c_f32_f16_e32 v215, s39, v117
	v_and_b32_e32 v117, s32, v117
	v_dot2c_f32_f16_e32 v214, s39, v149
	v_and_b32_e32 v149, s32, v149
	v_dot2c_f32_f16_e32 v211, s39, v117
	v_perm_b32 v148, v146, v150, s29
	v_dot2c_f32_f16_e32 v224, s37, v148
	v_and_b32_e32 v148, s32, v148
	v_dot2c_f32_f16_e32 v220, s37, v148
	v_perm_b32 v148, v146, v150, s30
	v_dot2c_f32_f16_e32 v225, s37, v148
	v_and_b32_e32 v148, s32, v148
	v_dot2c_f32_f16_e32 v221, s37, v148
	v_perm_b32 v148, v146, v150, s31
	v_perm_b32 v117, v146, v150, s33
	v_dot2c_f32_f16_e32 v223, s37, v117
	v_and_b32_e32 v117, s32, v117
	v_dot2c_f32_f16_e32 v222, s37, v148
	v_and_b32_e32 v148, s32, v148
	v_dot2c_f32_f16_e32 v219, s37, v117
	v_perm_b32 v207, v147, v151, s29
	v_dot2c_f32_f16_e32 v216, s37, v207
	v_and_b32_e32 v207, s32, v207
	v_dot2c_f32_f16_e32 v212, s37, v207
	v_perm_b32 v207, v147, v151, s30
	v_dot2c_f32_f16_e32 v217, s37, v207
	v_and_b32_e32 v207, s32, v207
	v_dot2c_f32_f16_e32 v213, s37, v207
	v_perm_b32 v207, v147, v151, s31
	v_perm_b32 v117, v147, v151, s33
	v_dot2c_f32_f16_e32 v215, s37, v117
	v_and_b32_e32 v117, s32, v117
	v_dot2c_f32_f16_e32 v214, s37, v207
	v_and_b32_e32 v207, s32, v207
	v_dot2c_f32_f16_e32 v211, s37, v117
	v_perm_b32 v145, v114, v118, s29
	v_dot2c_f32_f16_e32 v224, s35, v145
	v_and_b32_e32 v145, s32, v145
	v_dot2c_f32_f16_e32 v220, s35, v145
	v_perm_b32 v145, v114, v118, s30
	v_dot2c_f32_f16_e32 v225, s35, v145
	v_and_b32_e32 v145, s32, v145
	v_dot2c_f32_f16_e32 v221, s35, v145
	v_perm_b32 v145, v114, v118, s31
	v_dot2c_f32_f16_e32 v222, s35, v145
	v_and_b32_e32 v145, s32, v145
	v_perm_b32 v117, v114, v118, s33
	v_and_b32_e32 v209, s32, v117
	v_dot2c_f32_f16_e32 v223, s35, v117
	v_dot2c_f32_f16_e32 v219, s35, v209
	v_perm_b32 v253, v115, v119, s29
	v_dot2c_f32_f16_e32 v216, s35, v253
	v_and_b32_e32 v253, s32, v253
	v_dot2c_f32_f16_e32 v212, s35, v253
	v_perm_b32 v253, v115, v119, s30
	v_dot2c_f32_f16_e32 v217, s35, v253
	v_and_b32_e32 v253, s32, v253
	v_dot2c_f32_f16_e32 v213, s35, v253
	v_perm_b32 v253, v115, v119, s31
	v_perm_b32 v209, v115, v119, s33
	v_dot2c_f32_f16_e32 v215, s35, v209
	v_and_b32_e32 v209, s32, v209
	v_dot2c_f32_f16_e32 v214, s35, v253
	v_and_b32_e32 v253, s32, v253
	v_dot2c_f32_f16_e32 v211, s35, v209
	v_perm_b32 v117, v68, v72, s29
	v_dot2c_f32_f16_e32 v224, s4, v117
	v_and_b32_e32 v117, s32, v117
	v_dot2c_f32_f16_e32 v220, s4, v117
	v_perm_b32 v117, v68, v72, s30
	v_dot2c_f32_f16_e32 v225, s4, v117
	v_and_b32_e32 v117, s32, v117
	v_dot2c_f32_f16_e32 v221, s4, v117
	v_perm_b32 v117, v68, v72, s31
	v_dot2c_f32_f16_e32 v222, s4, v117
	v_and_b32_e32 v117, s32, v117
	v_perm_b32 v254, v68, v72, s33
	v_and_b32_e32 v254, s32, v254
	v_perm_b32 v209, v68, v72, s33
	v_dot2c_f32_f16_e32 v219, s4, v254
	v_dot2c_f32_f16_e32 v223, s4, v209
	v_perm_b32 v209, v69, v73, s29
	v_dot2c_f32_f16_e32 v216, s4, v209
	v_and_b32_e32 v209, s32, v209
	v_dot2c_f32_f16_e32 v212, s4, v209
	v_perm_b32 v209, v69, v73, s30
	v_dot2c_f32_f16_e32 v217, s4, v209
	v_and_b32_e32 v209, s32, v209
	v_dot2c_f32_f16_e32 v213, s4, v209
	v_perm_b32 v209, v69, v73, s31
	v_perm_b32 v254, v69, v73, s33
	v_dot2c_f32_f16_e32 v215, s4, v254
	s_waitcnt vmcnt(31)
	v_dot8_i32_i4 v68, v248, v62, 0
	v_dot8_i32_i4 v68, v250, v63, v68
	v_dot2c_f32_f16_e32 v210, s39, v149
	v_dot2c_f32_f16_e32 v218, s37, v148
	v_dot2c_f32_f16_e32 v210, s37, v207
	v_lshlrev_b32_e32 v68, 4, v68
	v_dot8_i32_i4 v68, v247, v62, v68
	s_waitcnt vmcnt(30)
	v_dot8_i32_i4 v62, v248, v58, 0
	v_dot8_i32_i4 v62, v250, v59, v62
	v_dot8_i32_i4 v68, v249, v63, v68
	v_dot2c_f32_f16_e32 v218, s35, v145
	v_dot2c_f32_f16_e32 v210, s35, v253
	v_lshlrev_b32_e32 v62, 4, v62
	v_dot8_i32_i4 v62, v247, v58, v62
	s_waitcnt vmcnt(29)
	v_dot8_i32_i4 v58, v248, v54, 0
	v_dot8_i32_i4 v58, v250, v55, v58
	v_dot8_i32_i4 v62, v249, v59, v62
	v_dot2c_f32_f16_e32 v214, s4, v209
	v_and_b32_e32 v209, s32, v209
	v_lshlrev_b32_e32 v58, 4, v58
	v_dot8_i32_i4 v58, v247, v54, v58
	s_waitcnt vmcnt(28)
	v_dot8_i32_i4 v54, v248, v50, 0
	v_dot8_i32_i4 v54, v250, v51, v54
	v_dot8_i32_i4 v58, v249, v55, v58
	v_dot2c_f32_f16_e32 v218, s4, v117
	v_dot2c_f32_f16_e32 v210, s4, v209
	v_lshlrev_b32_e32 v54, 4, v54
	v_dot8_i32_i4 v54, v247, v50, v54
	s_waitcnt vmcnt(27)
	v_dot8_i32_i4 v50, v248, v46, 0
	v_dot8_i32_i4 v50, v250, v47, v50
	v_dot8_i32_i4 v54, v249, v51, v54
	s_add_i32 s24, s25, 2
	s_cmp_lt_u32 s25, 5
	v_lshlrev_b32_e32 v50, 4, v50
	v_dot8_i32_i4 v50, v247, v46, v50
	s_waitcnt vmcnt(26)
	v_dot8_i32_i4 v46, v248, v42, 0
	v_dot8_i32_i4 v46, v250, v43, v46
	v_dot8_i32_i4 v50, v249, v47, v50
	v_cvt_f32_f16_e32 v116, v116
	s_nop 0
	v_lshlrev_b32_e32 v46, 4, v46
	v_dot8_i32_i4 v46, v247, v42, v46
	s_waitcnt vmcnt(25)
	v_dot8_i32_i4 v42, v248, v38, 0
	v_dot8_i32_i4 v42, v250, v39, v42
	v_dot8_i32_i4 v46, v249, v43, v46
	s_nop 1
	v_lshlrev_b32_e32 v42, 4, v42
	v_dot8_i32_i4 v42, v247, v38, v42
	s_waitcnt vmcnt(24)
	v_dot8_i32_i4 v38, v248, v30, 0
	v_dot8_i32_i4 v38, v250, v31, v38
	v_dot8_i32_i4 v42, v249, v39, v42
	s_nop 1
	v_lshlrev_b32_e32 v38, 4, v38
	v_dot8_i32_i4 v38, v247, v30, v38
	v_dot8_i32_i4 v38, v249, v31, v38
	s_waitcnt vmcnt(22)
	v_dot8_i32_i4 v31, v248, v22, 0
	v_dot8_i32_i4 v31, v250, v23, v31
	v_dot8_i32_i4 v30, v248, v34, 0
	v_dot8_i32_i4 v30, v250, v35, v30
	s_nop 0
	v_lshlrev_b32_e32 v31, 4, v31
	v_dot8_i32_i4 v31, v247, v22, v31
	v_dot8_i32_i4 v31, v249, v23, v31
	s_waitcnt vmcnt(20)
	v_dot8_i32_i4 v23, v248, v14, 0
	v_dot8_i32_i4 v23, v250, v15, v23
	v_dot8_i32_i4 v22, v248, v26, 0
	v_dot8_i32_i4 v22, v250, v27, v22
	s_nop 0
	v_lshlrev_b32_e32 v23, 4, v23
	v_dot8_i32_i4 v23, v247, v14, v23
	v_dot8_i32_i4 v23, v249, v15, v23
	s_waitcnt vmcnt(18)
	v_dot8_i32_i4 v15, v248, v6, 0
	v_dot8_i32_i4 v15, v250, v7, v15
	v_dot8_i32_i4 v14, v248, v18, 0
	v_dot8_i32_i4 v14, v250, v19, v14
	s_nop 0
	v_lshlrev_b32_e32 v15, 4, v15
	v_dot8_i32_i4 v15, v247, v6, v15
	v_dot8_i32_i4 v15, v249, v7, v15
	s_waitcnt vmcnt(17)
	v_dot8_i32_i4 v6, v248, v10, 0
	s_waitcnt vmcnt(16)
	v_dot8_i32_i4 v7, v248, v2, 0
	v_dot8_i32_i4 v6, v250, v11, v6
	v_dot8_i32_i4 v7, v250, v3, v7
	v_lshlrev_b32_e32 v30, 4, v30
	v_lshlrev_b32_e32 v22, 4, v22
	v_lshlrev_b32_e32 v14, 4, v14
	v_lshlrev_b32_e32 v6, 4, v6
	v_lshlrev_b32_e32 v7, 4, v7
	v_dot8_i32_i4 v30, v247, v34, v30
	v_dot8_i32_i4 v22, v247, v26, v22
	v_dot8_i32_i4 v14, v247, v18, v14
	v_dot8_i32_i4 v6, v247, v10, v6
	v_dot8_i32_i4 v7, v247, v2, v7
	v_dot8_i32_i4 v30, v249, v35, v30
	v_dot8_i32_i4 v22, v249, v27, v22
	v_dot8_i32_i4 v14, v249, v19, v14
	v_dot8_i32_i4 v6, v249, v11, v6
	v_dot8_i32_i4 v7, v249, v3, v7
	v_permlane32_swap_b32_e32 v68, v30
	v_permlane32_swap_b32_e32 v62, v31
	v_permlane32_swap_b32_e32 v58, v22
	v_permlane32_swap_b32_e32 v54, v23
	v_permlane32_swap_b32_e32 v50, v14
	v_permlane32_swap_b32_e32 v46, v15
	v_permlane32_swap_b32_e32 v42, v6
	v_permlane32_swap_b32_e32 v38, v7
	v_add_u32_e32 v2, v68, v30
	v_add_u32_e32 v3, v62, v31
	v_add_u32_e32 v10, v58, v22
	v_add_u32_e32 v11, v54, v23
	v_add_u32_e32 v14, v50, v14
	v_add_u32_e32 v15, v46, v15
	v_add_u32_e32 v6, v42, v6
	v_add_u32_e32 v7, v38, v7
	v_permlane16_swap_b32_e32 v2, v14
	v_permlane16_swap_b32_e32 v3, v15
	v_permlane16_swap_b32_e32 v10, v6
	v_permlane16_swap_b32_e32 v11, v7
	v_add_u32_e32 v2, v2, v14
	v_add_u32_e32 v3, v3, v15
	v_add_u32_e32 v6, v10, v6
	v_add_u32_e32 v7, v11, v7
	v_cndmask_b32_e64 v10, v6, v2, s[0:1]
	v_cndmask_b32_e64 v2, v2, v6, s[0:1]
	v_cndmask_b32_e64 v6, v7, v3, s[0:1]
	v_cndmask_b32_e64 v3, v3, v7, s[0:1]
	v_add_u32_dpp v2, v2, v10 quad_perm:[2,3,0,1] row_mask:0xf bank_mask:0xf bound_ctrl:1
	s_waitcnt lgkmcnt(0)
	ds_bpermute_b32 v7, v66, v71 offset:64
	v_add_u32_dpp v3, v3, v6 quad_perm:[2,3,0,1] row_mask:0xf bank_mask:0xf bound_ctrl:1
	v_cndmask_b32_e64 v6, v3, v2, s[2:3]
	v_cndmask_b32_e64 v2, v2, v3, s[2:3]
	ds_bpermute_b32 v3, v66, v70 offset:64
	v_add_f32_e32 v68, v252, v116
	v_add_u32_dpp v2, v2, v6 quad_perm:[1,0,3,2] row_mask:0xf bank_mask:0xf bound_ctrl:1
	v_and_b32_e32 v6, s32, v254
	v_dot2c_f32_f16_e32 v211, s4, v6
	v_add_u32_dpp v2, v2, v2 row_ror:8 row_mask:0xf bank_mask:0xf bound_ctrl:1
	ds_bpermute_b32 v6, v66, v67 offset:64
	s_nop 0
	v_add_u32_dpp v2, v2, v2 row_ror:4 row_mask:0xf bank_mask:0xf bound_ctrl:1
	v_cvt_f32_i32_e32 v2, v2
	v_add_f32_e32 v2, v251, v2
	v_mul_f32_e32 v2, v244, v2
	s_waitcnt lgkmcnt(1)
	v_mul_f32_e32 v2, v2, v3
	v_fma_f32 v3, |v2|, s28, 1.0
	v_rcp_f32_e32 v3, v3
	v_mul_f32_e32 v11, v2, v2
	v_mul_f32_e32 v11, 0xbf38aa3b, v11
	v_exp_f32_e32 v11, v11
	v_fmamk_f32 v10, v3, 0x3f07dc22, v227
	v_fmaak_f32 v10, v3, v10, 0x3f35f0e3
	v_fmaak_f32 v10, v3, v10, 0xbe11a98e
	v_fmaak_f32 v10, v3, v10, 0x3e027906
	v_mul_f32_e32 v3, v3, v10
	v_mul_f32_e32 v3, v11, v3
	v_mul_f32_e32 v10, v2, v3
	v_fma_f32 v3, -v2, v3, v2
	v_cmp_gt_f32_e64 s[4:5], 0, v2
	s_nop 1
	v_cndmask_b32_e64 v2, v3, v10, s[4:5]
	s_waitcnt lgkmcnt(0)
	v_mul_f32_e32 v2, v2, v6
	v_mul_f32_e32 v2, v2, v7
	v_fma_mixlo_f16 v2, v2, s16, 0
	v_and_b32_e32 v3, 0xffff, v2
	s_cselect_b64 s[4:5], -1, 0
	s_nop 0
	v_mov_b32_dpp v253, v3 quad_perm:[1,0,3,2] row_mask:0xf bank_mask:0xf
	v_lshl_or_b32 v254, v253, 16, v3
	v_cvt_f32_f16_e32 v66, v2
	v_readlane_b32 s5, v254, 0
	v_perm_b32 v14, v60, v64, s29
	s_nop 0
	v_dot2c_f32_f16_e32 v224, s5, v14
	v_and_b32_e32 v14, s32, v14
	v_dot2c_f32_f16_e32 v220, s5, v14
	v_perm_b32 v14, v60, v64, s30
	v_dot2c_f32_f16_e32 v225, s5, v14
	v_and_b32_e32 v14, s32, v14
	v_dot2c_f32_f16_e32 v221, s5, v14
	v_perm_b32 v14, v60, v64, s31
	v_perm_b32 v6, v60, v64, s33
	v_dot2c_f32_f16_e32 v223, s5, v6
	v_and_b32_e32 v6, s32, v6
	v_dot2c_f32_f16_e32 v222, s5, v14
	v_and_b32_e32 v14, s32, v14
	v_dot2c_f32_f16_e32 v219, s5, v6
	v_dot2c_f32_f16_e32 v218, s5, v14
	v_perm_b32 v14, v61, v65, s29
	v_dot2c_f32_f16_e32 v216, s5, v14
	v_and_b32_e32 v14, s32, v14
	v_dot2c_f32_f16_e32 v212, s5, v14
	v_perm_b32 v14, v61, v65, s30
	v_dot2c_f32_f16_e32 v217, s5, v14
	v_and_b32_e32 v14, s32, v14
	v_dot2c_f32_f16_e32 v213, s5, v14
	v_perm_b32 v14, v61, v65, s31
	v_perm_b32 v6, v61, v65, s33
	v_dot2c_f32_f16_e32 v214, s5, v14
	v_and_b32_e32 v14, s32, v14
	v_dot2c_f32_f16_e32 v215, s5, v6
	v_and_b32_e32 v6, s32, v6
	v_dot2c_f32_f16_e32 v210, s5, v14
	v_dot2c_f32_f16_e32 v211, s5, v6
	buffer_load_dwordx4 v[62:65], v194, s[80:83], s64 offen
	buffer_load_dwordx4 v[58:61], v194, s[80:83], s65 offen
	v_readlane_b32 s4, v254, 2
	v_perm_b32 v14, v52, v56, s29
	s_nop 0
	v_dot2c_f32_f16_e32 v224, s4, v14
	v_and_b32_e32 v14, s32, v14
	v_dot2c_f32_f16_e32 v220, s4, v14
	v_perm_b32 v14, v52, v56, s30
	v_dot2c_f32_f16_e32 v225, s4, v14
	v_and_b32_e32 v14, s32, v14
	v_dot2c_f32_f16_e32 v221, s4, v14
	v_perm_b32 v14, v52, v56, s31
	v_perm_b32 v6, v52, v56, s33
	v_dot2c_f32_f16_e32 v223, s4, v6
	v_and_b32_e32 v6, s32, v6
	v_dot2c_f32_f16_e32 v222, s4, v14
	v_and_b32_e32 v14, s32, v14
	v_dot2c_f32_f16_e32 v219, s4, v6
	v_dot2c_f32_f16_e32 v218, s4, v14
	v_perm_b32 v14, v53, v57, s29
	v_dot2c_f32_f16_e32 v216, s4, v14
	v_and_b32_e32 v14, s32, v14
	v_dot2c_f32_f16_e32 v212, s4, v14
	v_perm_b32 v14, v53, v57, s30
	v_dot2c_f32_f16_e32 v217, s4, v14
	v_and_b32_e32 v14, s32, v14
	v_dot2c_f32_f16_e32 v213, s4, v14
	v_perm_b32 v14, v53, v57, s31
	v_perm_b32 v6, v53, v57, s33
	v_dot2c_f32_f16_e32 v214, s4, v14
	v_and_b32_e32 v14, s32, v14
	v_dot2c_f32_f16_e32 v215, s4, v6
	v_and_b32_e32 v6, s32, v6
	v_dot2c_f32_f16_e32 v210, s4, v14
	v_dot2c_f32_f16_e32 v211, s4, v6
	buffer_load_dwordx4 v[54:57], v194, s[80:83], s66 offen
	buffer_load_dwordx4 v[50:53], v194, s[80:83], s67 offen
	v_readlane_b32 s4, v254, 16
	v_perm_b32 v14, v44, v48, s29
	s_nop 0
	v_dot2c_f32_f16_e32 v224, s4, v14
	v_and_b32_e32 v14, s32, v14
	v_dot2c_f32_f16_e32 v220, s4, v14
	v_perm_b32 v14, v44, v48, s30
	v_dot2c_f32_f16_e32 v225, s4, v14
	v_and_b32_e32 v14, s32, v14
	v_dot2c_f32_f16_e32 v221, s4, v14
	v_perm_b32 v14, v44, v48, s31
	v_perm_b32 v6, v44, v48, s33
	v_dot2c_f32_f16_e32 v223, s4, v6
	v_and_b32_e32 v6, s32, v6
	v_dot2c_f32_f16_e32 v222, s4, v14
	v_and_b32_e32 v14, s32, v14
	v_dot2c_f32_f16_e32 v219, s4, v6
	v_dot2c_f32_f16_e32 v218, s4, v14
	v_perm_b32 v14, v45, v49, s29
	v_dot2c_f32_f16_e32 v216, s4, v14
	v_and_b32_e32 v14, s32, v14
	v_dot2c_f32_f16_e32 v212, s4, v14
	v_perm_b32 v14, v45, v49, s30
	v_dot2c_f32_f16_e32 v217, s4, v14
	v_and_b32_e32 v14, s32, v14
	v_dot2c_f32_f16_e32 v213, s4, v14
	v_perm_b32 v14, v45, v49, s31
	v_perm_b32 v6, v45, v49, s33
	v_dot2c_f32_f16_e32 v214, s4, v14
	v_and_b32_e32 v14, s32, v14
	v_dot2c_f32_f16_e32 v215, s4, v6
	v_and_b32_e32 v6, s32, v6
	v_dot2c_f32_f16_e32 v210, s4, v14
	v_dot2c_f32_f16_e32 v211, s4, v6
	buffer_load_dwordx4 v[46:49], v194, s[80:83], s68 offen
	buffer_load_dwordx4 v[42:45], v194, s[80:83], s69 offen
	v_readlane_b32 s4, v254, 18
	v_perm_b32 v14, v32, v40, s29
	s_nop 0
	v_dot2c_f32_f16_e32 v224, s4, v14
	v_and_b32_e32 v14, s32, v14
	v_dot2c_f32_f16_e32 v220, s4, v14
	v_perm_b32 v14, v32, v40, s30
	v_dot2c_f32_f16_e32 v225, s4, v14
	v_and_b32_e32 v14, s32, v14
	v_dot2c_f32_f16_e32 v221, s4, v14
	v_perm_b32 v14, v32, v40, s31
	v_perm_b32 v6, v32, v40, s33
	v_dot2c_f32_f16_e32 v223, s4, v6
	v_and_b32_e32 v6, s32, v6
	v_dot2c_f32_f16_e32 v222, s4, v14
	v_and_b32_e32 v14, s32, v14
	v_dot2c_f32_f16_e32 v219, s4, v6
	v_dot2c_f32_f16_e32 v218, s4, v14
	v_perm_b32 v14, v33, v41, s29
	v_dot2c_f32_f16_e32 v216, s4, v14
	v_and_b32_e32 v14, s32, v14
	v_dot2c_f32_f16_e32 v212, s4, v14
	v_perm_b32 v14, v33, v41, s30
	v_dot2c_f32_f16_e32 v217, s4, v14
	v_and_b32_e32 v14, s32, v14
	v_dot2c_f32_f16_e32 v213, s4, v14
	v_perm_b32 v14, v33, v41, s31
	v_perm_b32 v6, v33, v41, s33
	v_dot2c_f32_f16_e32 v214, s4, v14
	v_and_b32_e32 v14, s32, v14
	v_dot2c_f32_f16_e32 v215, s4, v6
	v_and_b32_e32 v6, s32, v6
	v_dot2c_f32_f16_e32 v210, s4, v14
	v_dot2c_f32_f16_e32 v211, s4, v6
	buffer_load_dwordx4 v[38:41], v194, s[80:83], s70 offen
	buffer_load_dwordx4 v[30:33], v194, s[80:83], s71 offen
	v_readlane_b32 s4, v254, 32
	v_perm_b32 v14, v24, v36, s29
	s_nop 0
	v_dot2c_f32_f16_e32 v224, s4, v14
	v_and_b32_e32 v14, s32, v14
	v_dot2c_f32_f16_e32 v220, s4, v14
	v_perm_b32 v14, v24, v36, s30
	v_dot2c_f32_f16_e32 v225, s4, v14
	v_and_b32_e32 v14, s32, v14
	v_dot2c_f32_f16_e32 v221, s4, v14
	v_perm_b32 v14, v24, v36, s31
	v_perm_b32 v6, v24, v36, s33
	v_dot2c_f32_f16_e32 v223, s4, v6
	v_and_b32_e32 v6, s32, v6
	v_dot2c_f32_f16_e32 v222, s4, v14
	v_and_b32_e32 v14, s32, v14
	v_dot2c_f32_f16_e32 v219, s4, v6
	v_dot2c_f32_f16_e32 v218, s4, v14
	v_perm_b32 v14, v25, v37, s29
	v_dot2c_f32_f16_e32 v216, s4, v14
	v_and_b32_e32 v14, s32, v14
	v_dot2c_f32_f16_e32 v212, s4, v14
	v_perm_b32 v14, v25, v37, s30
	v_dot2c_f32_f16_e32 v217, s4, v14
	v_and_b32_e32 v14, s32, v14
	v_dot2c_f32_f16_e32 v213, s4, v14
	v_perm_b32 v14, v25, v37, s31
	v_perm_b32 v6, v25, v37, s33
	v_dot2c_f32_f16_e32 v214, s4, v14
	v_and_b32_e32 v14, s32, v14
	v_dot2c_f32_f16_e32 v215, s4, v6
	v_and_b32_e32 v6, s32, v6
	v_dot2c_f32_f16_e32 v210, s4, v14
	v_dot2c_f32_f16_e32 v211, s4, v6
	buffer_load_dwordx4 v[34:37], v194, s[80:83], s72 offen
	buffer_load_dwordx4 v[22:25], v194, s[80:83], s73 offen
	v_readlane_b32 s4, v254, 34
	v_perm_b32 v14, v16, v28, s29
	s_nop 0
	v_dot2c_f32_f16_e32 v224, s4, v14
	v_and_b32_e32 v14, s32, v14
	v_dot2c_f32_f16_e32 v220, s4, v14
	v_perm_b32 v14, v16, v28, s30
	v_dot2c_f32_f16_e32 v225, s4, v14
	v_and_b32_e32 v14, s32, v14
	v_dot2c_f32_f16_e32 v221, s4, v14
	v_perm_b32 v14, v16, v28, s31
	v_perm_b32 v6, v16, v28, s33
	v_dot2c_f32_f16_e32 v223, s4, v6
	v_and_b32_e32 v6, s32, v6
	v_dot2c_f32_f16_e32 v222, s4, v14
	v_and_b32_e32 v14, s32, v14
	v_dot2c_f32_f16_e32 v219, s4, v6
	v_dot2c_f32_f16_e32 v218, s4, v14
	v_perm_b32 v14, v17, v29, s29
	v_dot2c_f32_f16_e32 v216, s4, v14
	v_and_b32_e32 v14, s32, v14
; __device__ __forceinline__ void expert_tokens(const unsigned char* __restrict__ UV, const float* __restrict__ US, const float* __restrict__ VS, ...
;     ...
;         for (int bi = 0; bi < 128 / EB; bi += 2) {
;             EXP_STEP(A, bi);
;             if (bi == 0) { nsu0 = US[ni0]; nsu1 = US[ni1]; nsv0 = VS[ni0]; nsv1 = VS[ni1]; }
;             EXP_STEP(B, bi + 1);
;         }
	v_dot2c_f32_f16_e32 v212, s4, v14
	v_perm_b32 v14, v17, v29, s30
	v_dot2c_f32_f16_e32 v217, s4, v14
	v_and_b32_e32 v14, s32, v14
	v_dot2c_f32_f16_e32 v213, s4, v14
	v_perm_b32 v14, v17, v29, s31
	v_perm_b32 v6, v17, v29, s33
	v_dot2c_f32_f16_e32 v214, s4, v14
	v_and_b32_e32 v14, s32, v14
	v_dot2c_f32_f16_e32 v215, s4, v6
	v_and_b32_e32 v6, s32, v6
	v_dot2c_f32_f16_e32 v210, s4, v14
	v_dot2c_f32_f16_e32 v211, s4, v6
	buffer_load_dwordx4 v[26:29], v194, s[80:83], s74 offen
	buffer_load_dwordx4 v[14:17], v194, s[80:83], s75 offen
	v_readlane_b32 s4, v254, 48
	v_perm_b32 v11, v8, v20, s29
	s_nop 0
	v_dot2c_f32_f16_e32 v224, s4, v11
	v_and_b32_e32 v11, s32, v11
	v_dot2c_f32_f16_e32 v220, s4, v11
	v_perm_b32 v11, v8, v20, s30
	v_dot2c_f32_f16_e32 v225, s4, v11
	v_and_b32_e32 v11, s32, v11
	v_dot2c_f32_f16_e32 v221, s4, v11
	v_perm_b32 v11, v8, v20, s31
	v_perm_b32 v6, v8, v20, s33
	v_dot2c_f32_f16_e32 v223, s4, v6
	v_and_b32_e32 v6, s32, v6
	v_dot2c_f32_f16_e32 v222, s4, v11
	v_and_b32_e32 v11, s32, v11
	v_dot2c_f32_f16_e32 v219, s4, v6
	v_perm_b32 v10, v9, v21, s29
	v_dot2c_f32_f16_e32 v216, s4, v10
	v_and_b32_e32 v10, s32, v10
	v_dot2c_f32_f16_e32 v212, s4, v10
	v_perm_b32 v10, v9, v21, s30
	v_dot2c_f32_f16_e32 v217, s4, v10
	v_and_b32_e32 v10, s32, v10
	v_dot2c_f32_f16_e32 v213, s4, v10
	v_perm_b32 v10, v9, v21, s31
	v_perm_b32 v6, v9, v21, s33
	v_dot2c_f32_f16_e32 v214, s4, v10
	v_and_b32_e32 v10, s32, v10
	v_dot2c_f32_f16_e32 v215, s4, v6
	v_and_b32_e32 v6, s32, v6
	v_dot2c_f32_f16_e32 v218, s4, v11
	v_dot2c_f32_f16_e32 v210, s4, v10
	v_dot2c_f32_f16_e32 v211, s4, v6
	buffer_load_dwordx4 v[18:21], v194, s[80:83], s76 offen
	buffer_load_dwordx4 v[6:9], v194, s[80:83], s77 offen
	v_readlane_b32 s4, v254, 50
	v_perm_b32 v254, v4, v12, s29
	s_nop 0
	v_dot2c_f32_f16_e32 v224, s4, v254
	v_and_b32_e32 v254, s32, v254
	v_dot2c_f32_f16_e32 v220, s4, v254
	v_perm_b32 v254, v4, v12, s30
	v_dot2c_f32_f16_e32 v225, s4, v254
	v_and_b32_e32 v254, s32, v254
	v_dot2c_f32_f16_e32 v221, s4, v254
	v_perm_b32 v254, v4, v12, s31
	v_perm_b32 v3, v4, v12, s33
	v_dot2c_f32_f16_e32 v223, s4, v3
	v_and_b32_e32 v3, s32, v3
	v_dot2c_f32_f16_e32 v222, s4, v254
	v_and_b32_e32 v254, s32, v254
	v_dot2c_f32_f16_e32 v219, s4, v3
	v_perm_b32 v11, v5, v13, s29
	v_dot2c_f32_f16_e32 v216, s4, v11
	v_and_b32_e32 v11, s32, v11
	v_dot2c_f32_f16_e32 v212, s4, v11
	v_perm_b32 v11, v5, v13, s30
	v_dot2c_f32_f16_e32 v217, s4, v11
	v_and_b32_e32 v11, s32, v11
	v_dot2c_f32_f16_e32 v213, s4, v11
	v_perm_b32 v11, v5, v13, s31
	v_perm_b32 v3, v5, v13, s33
	v_dot2c_f32_f16_e32 v214, s4, v11
	v_and_b32_e32 v11, s32, v11
	v_dot2c_f32_f16_e32 v215, s4, v3
	v_and_b32_e32 v3, s32, v3
	v_dot2c_f32_f16_e32 v218, s4, v254
	v_dot2c_f32_f16_e32 v210, s4, v11
	v_dot2c_f32_f16_e32 v211, s4, v3
	buffer_load_dwordx4 v[10:13], v194, s[80:83], s78 offen
	buffer_load_dwordx4 v[2:5], v194, s[80:83], s79 offen
	v_add_f32_e32 v252, v68, v66
	s_add_i32 s21, s21, 32
	s_and_b64 vcc, exec, s[22:23]
	s_cbranch_vccnz .LBB0_1013
	s_waitcnt vmcnt(23)
	v_mov_b64_e32 v[158:159], v[112:113]
	v_mov_b64_e32 v[190:191], v[80:81]
	v_mov_b64_e32 v[186:187], v[76:77]
	v_mov_b64_e32 v[182:183], v[88:89]
	v_mov_b64_e32 v[178:179], v[84:85]
	v_mov_b64_e32 v[174:175], v[96:97]
	v_mov_b64_e32 v[170:171], v[92:93]
	v_mov_b64_e32 v[166:167], v[104:105]
	v_mov_b64_e32 v[162:163], v[100:101]
	v_mov_b64_e32 v[156:157], v[110:111]
	s_waitcnt vmcnt(22)
	v_mov_b64_e32 v[154:155], v[108:109]
	s_waitcnt vmcnt(21)
	v_mov_b64_e32 v[150:151], v[126:127]
	s_waitcnt vmcnt(20)
	v_mov_b64_e32 v[146:147], v[122:123]
	s_waitcnt vmcnt(19)
	v_mov_b64_e32 v[116:117], v[132:133]
	s_waitcnt vmcnt(18)
	v_mov_b64_e32 v[112:113], v[128:129]
	s_waitcnt vmcnt(17)
	v_mov_b64_e32 v[70:71], v[140:141]
	s_waitcnt vmcnt(16)
	v_mov_b64_e32 v[66:67], v[136:137]
	v_mov_b64_e32 v[188:189], v[78:79]
	v_mov_b64_e32 v[184:185], v[74:75]
	v_mov_b64_e32 v[180:181], v[86:87]
	v_mov_b64_e32 v[176:177], v[82:83]
	v_mov_b64_e32 v[172:173], v[94:95]
	v_mov_b64_e32 v[168:169], v[90:91]
	v_mov_b64_e32 v[164:165], v[102:103]
	v_mov_b64_e32 v[160:161], v[98:99]
	v_mov_b64_e32 v[152:153], v[106:107]
	v_mov_b64_e32 v[148:149], v[124:125]
	v_mov_b64_e32 v[144:145], v[120:121]
	v_mov_b64_e32 v[118:119], v[134:135]
	v_mov_b64_e32 v[114:115], v[130:131]
	v_mov_b64_e32 v[72:73], v[142:143]
	v_mov_b64_e32 v[68:69], v[138:139]
	s_mov_b32 s25, s24
	s_branch .LBB0_1019
